# attention phase: packed f32 VALU ops (v_pk_mul/add/fma_f32) replaced by scalar pairs of the same encoded size (doc 7.5 instruction selection; bit-identical arithmetic, code placement unchanged)
# baseline (speedup 1.0000x reference)
.LBB0_873:
	s_andn2_b64 vcc, exec, s[16:17]
	s_cbranch_vccnz .LBB0_877
	s_nop 0
	v_max_f32_e32 v124, v49, v49
	v_max_f32_e32 v125, v65, v65
	v_max_f32_e32 v124, v125, v124
	v_max_f32_e32 v125, v50, v50
	v_max_f32_e32 v126, v66, v66
	v_max_f32_e32 v125, v126, v125
	v_max_f32_e32 v126, v51, v51
	v_max_f32_e32 v127, v67, v67
	v_max3_f32 v124, v64, v48, v124
	v_max_f32_e32 v126, v127, v126
	v_max3_f32 v124, v124, v125, v126
	v_max_f32_e32 v125, v52, v52
	v_max_f32_e32 v126, v68, v68
	v_max_f32_e32 v125, v126, v125
	v_max_f32_e32 v126, v53, v53
	v_max_f32_e32 v127, v69, v69
	v_max_f32_e32 v126, v127, v126
	v_max3_f32 v124, v124, v125, v126
	v_max_f32_e32 v125, v54, v54
	v_max_f32_e32 v126, v70, v70
	v_max_f32_e32 v125, v126, v125
	v_max_f32_e32 v126, v55, v55
	v_max_f32_e32 v127, v71, v71
	v_max_f32_e32 v126, v127, v126
	v_max3_f32 v124, v124, v125, v126
	v_max_f32_e32 v125, v56, v56
	v_max_f32_e32 v126, v72, v72
	v_max_f32_e32 v125, v126, v125
	v_max_f32_e32 v126, v57, v57
	v_max_f32_e32 v127, v73, v73
	v_max_f32_e32 v126, v127, v126
	v_max3_f32 v124, v124, v125, v126
	v_max_f32_e32 v125, v58, v58
	v_max_f32_e32 v126, v74, v74
	v_max_f32_e32 v125, v126, v125
	v_max_f32_e32 v126, v59, v59
	v_max_f32_e32 v127, v75, v75
	v_max_f32_e32 v126, v127, v126
	v_max3_f32 v124, v124, v125, v126
	v_max_f32_e32 v125, v60, v60
	v_max_f32_e32 v126, v76, v76
	v_max_f32_e32 v125, v126, v125
	v_max_f32_e32 v126, v61, v61
	v_max_f32_e32 v127, v77, v77
	v_max_f32_e32 v126, v127, v126
	v_max3_f32 v124, v124, v125, v126
	v_max_f32_e32 v125, v62, v62
	v_max_f32_e32 v126, v78, v78
	v_max_f32_e32 v125, v126, v125
	v_max_f32_e32 v126, v63, v63
	v_max_f32_e32 v127, v79, v79
	v_max_f32_e32 v126, v127, v126
	v_max3_f32 v124, v124, v125, v126
	v_mov_b32_e32 v125, v124
	s_nop 1
	v_permlane32_swap_b32_e32 v124, v125
	v_max_f32_e32 v125, v125, v125
	v_max_f32_e32 v124, v124, v124
	v_max_f32_e32 v124, v124, v125
	s_and_b64 vcc, exec, s[40:41]
	v_max_f32_e32 v125, 0, v124
	s_cbranch_vccnz .LBB0_876
	v_exp_f32_e64 v126, -v125
	s_nop 0
	v_mul_f32_e32 v46, v46, v126
	v_mul_f32_e32 v47, v47, v126
	v_mul_f32_e32 v44, v44, v126
	v_mul_f32_e32 v45, v45, v126
	v_mul_f32_e32 v42, v42, v126
	v_mul_f32_e32 v43, v43, v126
	v_mul_f32_e32 v40, v40, v126
	v_mul_f32_e32 v41, v41, v126
	v_mul_f32_e32 v38, v38, v126
	v_mul_f32_e32 v39, v39, v126
	v_mul_f32_e32 v36, v36, v126
	v_mul_f32_e32 v37, v37, v126
	v_mul_f32_e32 v34, v34, v126
	v_mul_f32_e32 v35, v35, v126
	v_mul_f32_e32 v32, v32, v126
	v_mul_f32_e32 v33, v33, v126
	v_mul_f32_e32 v14, v14, v126
	v_mul_f32_e32 v15, v15, v126
	v_mul_f32_e32 v12, v12, v126
	v_mul_f32_e32 v13, v13, v126
	v_mul_f32_e32 v10, v10, v126
	v_mul_f32_e32 v11, v11, v126
	v_mul_f32_e32 v8, v8, v126
	v_mul_f32_e32 v9, v9, v126
	v_mul_f32_e32 v6, v6, v126
	v_mul_f32_e32 v7, v7, v126
	v_mul_f32_e32 v4, v4, v126
	v_mul_f32_e32 v5, v5, v126
	v_mul_f32_e32 v2, v2, v126
	v_mul_f32_e32 v3, v3, v126
	v_mul_f32_e32 v0, v0, v126
	v_mul_f32_e32 v1, v1, v126
	v_mul_f32_e32 v113, v113, v126

; __device__ __forceinline__ unsigned cvt_pk_bf16(float lo, float hi) { f32x2 v = {lo, hi}; bf16x2_t b = __builtin_convertvector(v, bf16x2_t); return __builtin_bit_cast(unsigned, b); }
; __device__ __forceinline__ float swapsum(float a) { auto rr = __builtin_amdgcn_permlane32_swap(__float_as_uint(a), __float_as_uint(a), false, false); return __uint_as_float(rr[0]) + __uint_as_float(rr[1]); }
;     ...
;     l = swapsum(l);
;     if (SWA) { const float sk = sink_l2 + (ALIBI ? slope_l2 * (float)(pos[qidx] - pos_ref) : 0.f);
;         const float mnew = fmaxf(m, sk), f = __builtin_amdgcn_exp2f(m - mnew); l = l * f + __builtin_amdgcn_exp2f(sk - mnew);
; #pragma unroll
;         for (int i = 0; i < 16; ++i) { ot[0][i] *= f; ot[1][i] *= f; } }
;     const float inv = 1.f / l;
;     ...
;     else { bf16_t* op = (bf16_t*)outp + (size_t)qidx * opitch + 4 * hf + hsel * 64;
; #pragma unroll
;         for (int db = 0; db < 2; ++db)
; #pragma unroll
;             for (int g = 0; g < 4; ++g) *(u32x2*)(op + 32 * db + 8 * g) = (u32x2){cvt_pk_bf16(ot[db][4 * g] * inv, ot[db][4 * g + 1] * inv), cvt_pk_bf16(ot[db][4 * g + 2] * inv, ot[db][4 * g + 3] * inv)}; }
.LBB0_892:
	s_or_b64 exec, exec, s[14:15]
	s_mulk_i32 s29, 0xa00
	v_mov_b32_e32 v16, v113
	s_add_u32 s14, s13, s29
	s_nop 0
	v_permlane32_swap_b32_e32 v113, v16
	s_addc_u32 s15, s31, 0
	s_lshl_b32 s16, s42, 1
	v_add_f32_e32 v16, v113, v16
	s_add_u32 s14, s14, s16
	v_div_scale_f32 v17, s[16:17], v16, v16, 1.0
	v_rcp_f32_e32 v18, v17
	s_addc_u32 s15, s15, 0
	v_fma_f32 v19, -v17, v18, 1.0
	v_fmac_f32_e32 v18, v19, v18
	v_div_scale_f32 v19, vcc, 1.0, v16, 1.0
	v_mul_f32_e32 v20, v19, v18
	v_fma_f32 v21, -v17, v20, v19
	v_fmac_f32_e32 v20, v21, v18
	v_fma_f32 v17, -v17, v20, v19
	v_div_fmas_f32 v17, v17, v18, v20
	v_mov_b64_e32 v[18:19], s[14:15]
	s_movk_i32 s14, 0xa00
	v_div_fixup_f32 v16, v17, v16, 1.0
	v_mad_i64_i32 v[18:19], s[14:15], v28, s14, v[18:19]
	v_lshlrev_b32_e32 v20, 1, v30
	v_mov_b32_e32 v21, v31
	v_lshl_add_u64 v[18:19], v[18:19], 0, v[20:21]
	v_mul_f32_e32 v20, v32, v16
	v_mul_f32_e32 v21, v33, v16
	v_mul_f32_e32 v22, v34, v16
	v_mul_f32_e32 v23, v35, v16
	v_mul_f32_e32 v0, v0, v16
	v_mul_f32_e32 v1, v1, v16
	v_mul_f32_e32 v2, v2, v16
	v_mul_f32_e32 v3, v3, v16
	v_cvt_pk_bf16_f32 v32, v20, v21
	v_cvt_pk_bf16_f32 v33, v22, v23
	v_cvt_pk_bf16_f32 v34, v0, v1
	v_cvt_pk_bf16_f32 v35, v2, v3
	v_mul_f32_e32 v20, v36, v16
	v_mul_f32_e32 v21, v37, v16
	v_mul_f32_e32 v22, v38, v16
	v_mul_f32_e32 v23, v39, v16
	v_mul_f32_e32 v0, v4, v16
	v_mul_f32_e32 v1, v5, v16
	v_mul_f32_e32 v2, v6, v16
	v_mul_f32_e32 v3, v7, v16
	v_cvt_pk_bf16_f32 v36, v20, v21
	v_cvt_pk_bf16_f32 v37, v22, v23
	v_cvt_pk_bf16_f32 v38, v0, v1
	v_cvt_pk_bf16_f32 v39, v2, v3
	v_mul_f32_e32 v20, v40, v16
	v_mul_f32_e32 v21, v41, v16
	v_mul_f32_e32 v22, v42, v16
	v_mul_f32_e32 v23, v43, v16
	v_mul_f32_e32 v0, v8, v16
	v_mul_f32_e32 v1, v9, v16
	v_mul_f32_e32 v2, v10, v16
	v_mul_f32_e32 v3, v11, v16
	v_cvt_pk_bf16_f32 v40, v20, v21
	v_cvt_pk_bf16_f32 v41, v22, v23
	v_cvt_pk_bf16_f32 v42, v0, v1
	v_cvt_pk_bf16_f32 v43, v2, v3
	v_mul_f32_e32 v20, v44, v16
	v_mul_f32_e32 v21, v45, v16
	v_mul_f32_e32 v22, v46, v16
	v_mul_f32_e32 v23, v47, v16
	v_mul_f32_e32 v0, v12, v16
	v_mul_f32_e32 v1, v13, v16
	v_mul_f32_e32 v2, v14, v16
	v_mul_f32_e32 v3, v15, v16
	v_cvt_pk_bf16_f32 v44, v20, v21
	v_cvt_pk_bf16_f32 v45, v22, v23
	v_cvt_pk_bf16_f32 v46, v0, v1
	v_cvt_pk_bf16_f32 v47, v2, v3
	s_nop 1
	v_permlane32_swap_b32_e32 v32, v34
	v_permlane32_swap_b32_e32 v33, v35
	v_permlane32_swap_b32_e32 v36, v38
	v_permlane32_swap_b32_e32 v37, v39
	v_permlane32_swap_b32_e32 v40, v42
	v_permlane32_swap_b32_e32 v41, v43
	v_permlane32_swap_b32_e32 v44, v46
	v_permlane32_swap_b32_e32 v45, v47
	v_mbcnt_lo_u32_b32 v22, -1, 0
	v_mbcnt_hi_u32_b32 v22, -1, v22
	v_lshrrev_b32_e32 v22, 5, v22
	v_mul_u32_u24_e32 v22, 56, v22
	v_add_co_u32_e32 v18, vcc, v18, v22
	s_nop 1
	v_addc_co_u32_e32 v19, vcc, 0, v19, vcc
	global_store_dwordx4 v[18:19], v[32:35], off
	global_store_dwordx4 v[18:19], v[36:39], off offset:16
	global_store_dwordx4 v[18:19], v[40:43], off offset:32
	global_store_dwordx4 v[18:19], v[44:47], off offset:48
	s_andn2_b64 vcc, exec, s[10:11]
	s_cbranch_vccz .LBB0_894

;     ...
;         int pm0 = 0, pm1 = 0; if (DESC) { pm0 = pmaxpre[2 * t]; pm1 = pmaxpre[2 * t + 1]; }
.LBB0_931:
	s_lshr_b32 s64, s58, 2
	s_and_b32 s65, s64, 63
	s_add_i32 s69, s65, 1
	v_readlane_b32 s70, v195, s65
	v_readlane_b32 s71, v194, s65
	v_readlane_b32 s65, v195, s69
	v_readlane_b32 s69, v194, s69
	s_nop 1
	s_cmp_lt_u32 s64, 64
	s_cselect_b32 s70, s70, s71
	s_cselect_b32 s65, s65, s69
	v_mov_b32_e32 v30, s70
	v_mov_b32_e32 v32, s65
	s_mov_b32 s68, s44
	s_add_i32 s44, s67, 1
	s_cmp_gt_i32 s44, s66
	s_cselect_b64 s[44:45], -1, 0
	s_or_b64 s[70:71], s[44:45], s[60:61]
	s_or_b64 s[70:71], s[70:71], s[62:63]
	s_and_b64 vcc, exec, s[70:71]
	s_cbranch_vccnz .LBB0_933
	v_sub_u32_e32 v32, v32, v142
	v_cvt_f32_i32_e32 v32, v32
	v_mul_f32_e32 v202, v143, v32
	v_add_f32_e32 v32, v110, v202
	v_add_f32_e32 v33, v111, v203
	s_nop 0
	v_cmp_lt_f32_e32 vcc, v32, v33
	s_cmp_eq_u64 vcc, exec
	s_cselect_b64 s[60:61], -1, 0

.LBB0_938:
	s_andn2_b64 vcc, exec, s[64:65]
	s_cbranch_vccnz .LBB0_942
	s_nop 0
	v_max_f32_e32 v32, v63, v63
	v_max_f32_e32 v33, v79, v79
	v_max_f32_e32 v32, v33, v32
	v_max_f32_e32 v33, v64, v64
	v_max_f32_e32 v34, v80, v80
	v_max_f32_e32 v33, v34, v33
	v_max_f32_e32 v34, v65, v65
	v_max_f32_e32 v35, v81, v81
	v_max3_f32 v32, v78, v62, v32
	v_max_f32_e32 v34, v35, v34
	v_max3_f32 v32, v32, v33, v34
	v_max_f32_e32 v33, v66, v66
	v_max_f32_e32 v34, v82, v82
	v_max_f32_e32 v33, v34, v33
	v_max_f32_e32 v34, v67, v67
	v_max_f32_e32 v35, v83, v83
	v_max_f32_e32 v34, v35, v34
	v_max3_f32 v32, v32, v33, v34
	v_max_f32_e32 v33, v68, v68
	v_max_f32_e32 v34, v84, v84
	v_max_f32_e32 v33, v34, v33
	v_max_f32_e32 v34, v69, v69
	v_max_f32_e32 v35, v85, v85
	v_max_f32_e32 v34, v35, v34
	v_max3_f32 v32, v32, v33, v34
	v_max_f32_e32 v33, v70, v70
	v_max_f32_e32 v34, v86, v86
	v_max_f32_e32 v33, v34, v33
	v_max_f32_e32 v34, v71, v71
	v_max_f32_e32 v35, v87, v87
	v_max_f32_e32 v34, v35, v34
	v_max3_f32 v32, v32, v33, v34
	v_max_f32_e32 v33, v72, v72
	v_max_f32_e32 v34, v88, v88
	v_max_f32_e32 v33, v34, v33
	v_max_f32_e32 v34, v73, v73
	v_max_f32_e32 v35, v89, v89
	v_max_f32_e32 v34, v35, v34
	v_max3_f32 v32, v32, v33, v34
	v_max_f32_e32 v33, v74, v74
	v_max_f32_e32 v34, v90, v90
	v_max_f32_e32 v33, v34, v33
	v_max_f32_e32 v34, v75, v75
	v_max_f32_e32 v35, v91, v91
	v_max_f32_e32 v34, v35, v34
	v_max3_f32 v32, v32, v33, v34
	v_max_f32_e32 v33, v76, v76
	v_max_f32_e32 v34, v92, v92
	v_max_f32_e32 v33, v34, v33
	v_max_f32_e32 v34, v77, v77
	v_max_f32_e32 v35, v93, v93
	v_max_f32_e32 v34, v35, v34
	v_max3_f32 v32, v32, v33, v34
	v_mov_b32_e32 v33, v32
	s_nop 1
	v_permlane32_swap_b32_e32 v32, v33
	v_max_f32_e32 v33, v33, v33
	v_max_f32_e32 v32, v32, v32
	v_max_f32_e32 v32, v32, v33
	s_and_b64 vcc, exec, s[44:45]
	v_max_f32_e32 v33, 0, v32
	s_cbranch_vccnz .LBB0_941
	v_exp_f32_e64 v34, -v33
	s_nop 0
	v_mul_f32_e32 v60, v60, v34
	v_mul_f32_e32 v61, v61, v34
	v_mul_f32_e32 v58, v58, v34
	v_mul_f32_e32 v59, v59, v34
	v_mul_f32_e32 v56, v56, v34
	v_mul_f32_e32 v57, v57, v34
	v_mul_f32_e32 v54, v54, v34
	v_mul_f32_e32 v55, v55, v34
	v_mul_f32_e32 v52, v52, v34
	v_mul_f32_e32 v53, v53, v34
	v_mul_f32_e32 v50, v50, v34
	v_mul_f32_e32 v51, v51, v34
	v_mul_f32_e32 v48, v48, v34
	v_mul_f32_e32 v49, v49, v34
	v_mul_f32_e32 v46, v46, v34
	v_mul_f32_e32 v47, v47, v34
	v_mul_f32_e32 v14, v14, v34
	v_mul_f32_e32 v15, v15, v34
	v_mul_f32_e32 v12, v12, v34
	v_mul_f32_e32 v13, v13, v34
	v_mul_f32_e32 v10, v10, v34
	v_mul_f32_e32 v11, v11, v34
	v_mul_f32_e32 v8, v8, v34
	v_mul_f32_e32 v9, v9, v34
	v_mul_f32_e32 v6, v6, v34
	v_mul_f32_e32 v7, v7, v34
	v_mul_f32_e32 v4, v4, v34
	v_mul_f32_e32 v5, v5, v34
	v_mul_f32_e32 v2, v2, v34
	v_mul_f32_e32 v3, v3, v34
	v_mul_f32_e32 v0, v0, v34
	v_mul_f32_e32 v1, v1, v34
	v_mul_f32_e32 v107, v107, v34

.LBB0_948:
	v_sub_u32_e32 v30, v30, v142
	v_cvt_f32_i32_e32 v30, v30
	v_mul_f32_e32 v202, v143, v30
	v_add_f32_e32 v32, v110, v202
	v_add_f32_e32 v33, v111, v203
	s_nop 0
	v_cmp_lt_f32_e32 vcc, v32, v33
	s_cmp_eq_u64 vcc, exec
	s_cselect_b64 s[60:61], -1, 0
	s_or_b64 s[44:45], s[44:45], s[60:61]
	s_and_b64 vcc, exec, s[44:45]
	s_cbranch_vccnz .LBB0_945

.LBB0_953:
	s_andn2_b64 vcc, exec, s[64:65]
	s_cbranch_vccnz .LBB0_957
	s_nop 1
	v_max_f32_e32 v30, v63, v63
	v_max_f32_e32 v32, v79, v79
	v_max_f32_e32 v30, v32, v30
	v_max_f32_e32 v32, v64, v64
	v_max_f32_e32 v33, v80, v80
	v_max_f32_e32 v32, v33, v32
	v_max_f32_e32 v33, v65, v65
	v_max_f32_e32 v34, v81, v81
	v_max3_f32 v30, v78, v62, v30
	v_max_f32_e32 v33, v34, v33
	v_max3_f32 v30, v30, v32, v33
	v_max_f32_e32 v32, v66, v66
	v_max_f32_e32 v33, v82, v82
	v_max_f32_e32 v32, v33, v32
	v_max_f32_e32 v33, v67, v67
	v_max_f32_e32 v34, v83, v83
	v_max_f32_e32 v33, v34, v33
	v_max3_f32 v30, v30, v32, v33
	v_max_f32_e32 v32, v68, v68
	v_max_f32_e32 v33, v84, v84
	v_max_f32_e32 v32, v33, v32
	v_max_f32_e32 v33, v69, v69
	v_max_f32_e32 v34, v85, v85
	v_max_f32_e32 v33, v34, v33
	v_max3_f32 v30, v30, v32, v33
	v_max_f32_e32 v32, v70, v70
	v_max_f32_e32 v33, v86, v86
	v_max_f32_e32 v32, v33, v32
	v_max_f32_e32 v33, v71, v71
	v_max_f32_e32 v34, v87, v87
	v_max_f32_e32 v33, v34, v33
	v_max3_f32 v30, v30, v32, v33
	v_max_f32_e32 v32, v72, v72
	v_max_f32_e32 v33, v88, v88
	v_max_f32_e32 v32, v33, v32
	v_max_f32_e32 v33, v73, v73
	v_max_f32_e32 v34, v89, v89
	v_max_f32_e32 v33, v34, v33
	v_max3_f32 v30, v30, v32, v33
	v_max_f32_e32 v32, v74, v74
	v_max_f32_e32 v33, v90, v90
	v_max_f32_e32 v32, v33, v32
	v_max_f32_e32 v33, v75, v75
	v_max_f32_e32 v34, v91, v91
	v_max_f32_e32 v33, v34, v33
	v_max3_f32 v30, v30, v32, v33
	v_max_f32_e32 v32, v76, v76
	v_max_f32_e32 v33, v92, v92
	v_max_f32_e32 v32, v33, v32
	v_max_f32_e32 v33, v77, v77
	v_max_f32_e32 v34, v93, v93
	v_max_f32_e32 v33, v34, v33
	v_max3_f32 v30, v30, v32, v33
	v_mov_b32_e32 v32, v30
	s_nop 1
	v_permlane32_swap_b32_e32 v30, v32
	v_max_f32_e32 v32, v32, v32
	v_max_f32_e32 v30, v30, v30
	v_max_f32_e32 v30, v30, v32
	s_and_b64 vcc, exec, s[44:45]
	v_max_f32_e32 v32, 0, v30
	s_cbranch_vccnz .LBB0_956
	v_exp_f32_e64 v34, -v32
	s_nop 0
	v_mul_f32_e32 v60, v60, v34
	v_mul_f32_e32 v61, v61, v34
	v_mul_f32_e32 v58, v58, v34
	v_mul_f32_e32 v59, v59, v34
	v_mul_f32_e32 v56, v56, v34
	v_mul_f32_e32 v57, v57, v34
	v_mul_f32_e32 v54, v54, v34
	v_mul_f32_e32 v55, v55, v34
	v_mul_f32_e32 v52, v52, v34
	v_mul_f32_e32 v53, v53, v34
	v_mul_f32_e32 v50, v50, v34
	v_mul_f32_e32 v51, v51, v34
	v_mul_f32_e32 v48, v48, v34
	v_mul_f32_e32 v49, v49, v34
	v_mul_f32_e32 v46, v46, v34
	v_mul_f32_e32 v47, v47, v34
	v_mul_f32_e32 v14, v14, v34
	v_mul_f32_e32 v15, v15, v34
	v_mul_f32_e32 v12, v12, v34
	v_mul_f32_e32 v13, v13, v34
	v_mul_f32_e32 v10, v10, v34
	v_mul_f32_e32 v11, v11, v34
	v_mul_f32_e32 v8, v8, v34
	v_mul_f32_e32 v9, v9, v34
	v_mul_f32_e32 v6, v6, v34
	v_mul_f32_e32 v7, v7, v34
	v_mul_f32_e32 v4, v4, v34
	v_mul_f32_e32 v5, v5, v34
	v_mul_f32_e32 v2, v2, v34
	v_mul_f32_e32 v3, v3, v34
	v_mul_f32_e32 v0, v0, v34
	v_mul_f32_e32 v1, v1, v34
	v_mul_f32_e32 v107, v107, v34

; #define LAS __attribute__((address_space(3)))
; __device__ __forceinline__ float swapsum(float a) { auto rr = __builtin_amdgcn_permlane32_swap(__float_as_uint(a), __float_as_uint(a), false, false); return __uint_as_float(rr[0]) + __uint_as_float(rr[1]); }
; __device__ __forceinline__ void lds_barrier() { asm volatile("s_waitcnt lgkmcnt(0)\n\ts_barrier" ::: "memory"); }
;     ...
;     if (MODE == 3) {
;         LAS float* xch = (LAS float*)(lds + XCH) + wq * 64 + lane;
;         if (mp) {
; #pragma unroll
;             for (int i = 0; i < 32; ++i) xch[i * 256] = ot[i >> 4][i & 15] * inv; }
;         lds_barrier();
;         if (!mp) {
;             float o[32]; float ss = 0.f;
; #pragma unroll
;             for (int i = 0; i < 32; ++i) { o[i] = ot[i >> 4][i & 15] * inv - lam * xch[i * 256]; ss += o[i] * o[i]; }
;             const float rs = __builtin_amdgcn_rsqf(swapsum(ss) * (1.f / 64.f) + 1e-6f);
.LBB0_973:
	s_waitcnt lgkmcnt(0)
	s_barrier
	s_andn2_b64 vcc, exec, s[36:37]
	s_cbranch_vccnz .LBB0_918
	s_waitcnt vmcnt(3)
	ds_read2st64_b32 v[26:27], v16 offset1:4
	ds_read2st64_b32 v[32:33], v16 offset0:8 offset1:12
	ds_read2st64_b32 v[34:35], v16 offset0:16 offset1:20
	ds_read2st64_b32 v[36:37], v16 offset0:24 offset1:28
	ds_read2st64_b32 v[38:39], v16 offset0:32 offset1:36
	ds_read2st64_b32 v[40:41], v16 offset0:40 offset1:44
	ds_read2st64_b32 v[42:43], v16 offset0:48 offset1:52
	ds_read2st64_b32 v[44:45], v16 offset0:56 offset1:60
	ds_read2st64_b32 v[62:63], v16 offset0:64 offset1:68
	ds_read2st64_b32 v[64:65], v16 offset0:72 offset1:76
	ds_read2st64_b32 v[66:67], v16 offset0:80 offset1:84
	ds_read2st64_b32 v[68:69], v16 offset0:88 offset1:92
	ds_read2st64_b32 v[70:71], v16 offset0:96 offset1:100
	ds_read2st64_b32 v[72:73], v16 offset0:104 offset1:108
	ds_read2st64_b32 v[18:19], v16 offset0:112 offset1:116
	ds_read2st64_b32 v[16:17], v16 offset0:120 offset1:124
	s_mulk_i32 s28, 0xa00
	s_add_u32 s4, s13, s28
	s_addc_u32 s21, s31, 0
	s_add_u32 s40, s4, s56
	s_addc_u32 s41, s21, s57
	s_waitcnt lgkmcnt(0)
	v_mul_f32_e32 v16, v28, v16
	v_mul_f32_e32 v17, v29, v17
	s_movk_i32 s4, 0xa00
	v_pk_fma_f32 v[16:17], v[14:15], v[20:21], v[16:17] op_sel_hi:[1,0,1] neg_lo:[0,0,1] neg_hi:[0,0,1]
	v_mov_b64_e32 v[14:15], s[40:41]
	v_mul_f32_e32 v18, v28, v18
	v_mul_f32_e32 v19, v29, v19
	v_mad_u64_u32 v[14:15], s[28:29], v109, s4, v[14:15]
	v_ashrrev_i32_e32 v109, 31, v108
	v_pk_fma_f32 v[12:13], v[12:13], v[20:21], v[18:19] op_sel_hi:[1,0,1] neg_lo:[0,0,1] neg_hi:[0,0,1]
	v_lshl_add_u64 v[18:19], v[108:109], 2, s[10:11]
	global_load_dwordx4 v[212:215], v[18:19], off
	global_load_dwordx4 v[216:219], v[18:19], off offset:32
	global_load_dwordx4 v[220:223], v[18:19], off offset:64
	global_load_dwordx4 v[224:227], v[18:19], off offset:96
	global_load_dwordx4 v[228:231], v[18:19], off offset:128
	global_load_dwordx4 v[232:235], v[18:19], off offset:160
	global_load_dwordx4 v[236:239], v[18:19], off offset:192
	global_load_dwordx4 v[240:243], v[18:19], off offset:224
	v_mul_f32_e32 v26, v28, v26
	v_mul_f32_e32 v27, v29, v27
	v_mul_f32_e32 v32, v28, v32
	v_mul_f32_e32 v33, v29, v33
	v_pk_fma_f32 v[26:27], v[46:47], v[20:21], v[26:27] op_sel_hi:[1,0,1] neg_lo:[0,0,1] neg_hi:[0,0,1]
	v_pk_fma_f32 v[32:33], v[48:49], v[20:21], v[32:33] op_sel_hi:[1,0,1] neg_lo:[0,0,1] neg_hi:[0,0,1]
	v_mul_f32_e32 v30, v27, v27
	v_pk_fma_f32 v[46:47], v[26:27], v[26:27], v[30:31] op_sel_hi:[1,1,0]
	v_mul_f32_e32 v30, v33, v33
	v_fmac_f32_e32 v46, v32, v32
	v_fmac_f32_e32 v47, v33, v33
	v_mul_f32_e32 v34, v28, v34
	v_mul_f32_e32 v35, v29, v35
	v_add_f32_e32 v46, v46, v30
	v_add_f32_e32 v47, v47, v30
	v_pk_fma_f32 v[34:35], v[50:51], v[20:21], v[34:35] op_sel_hi:[1,0,1] neg_lo:[0,0,1] neg_hi:[0,0,1]
	v_mul_f32_e32 v36, v28, v36
	v_mul_f32_e32 v37, v29, v37
	v_fmac_f32_e32 v46, v34, v34
	v_fmac_f32_e32 v47, v35, v35
	v_mul_f32_e32 v30, v35, v35
	v_pk_fma_f32 v[36:37], v[52:53], v[20:21], v[36:37] op_sel_hi:[1,0,1] neg_lo:[0,0,1] neg_hi:[0,0,1]
	v_add_f32_e32 v46, v46, v30
	v_add_f32_e32 v47, v47, v30
	v_mul_f32_e32 v30, v37, v37
	v_fmac_f32_e32 v46, v36, v36
	v_fmac_f32_e32 v47, v37, v37
	v_mul_f32_e32 v38, v28, v38
	v_mul_f32_e32 v39, v29, v39
	v_add_f32_e32 v46, v46, v30
	v_add_f32_e32 v47, v47, v30
	v_pk_fma_f32 v[38:39], v[54:55], v[20:21], v[38:39] op_sel_hi:[1,0,1] neg_lo:[0,0,1] neg_hi:[0,0,1]
	v_mul_f32_e32 v40, v28, v40
	v_mul_f32_e32 v41, v29, v41
	v_fmac_f32_e32 v46, v38, v38
	v_fmac_f32_e32 v47, v39, v39
	v_mul_f32_e32 v30, v39, v39
	v_pk_fma_f32 v[40:41], v[56:57], v[20:21], v[40:41] op_sel_hi:[1,0,1] neg_lo:[0,0,1] neg_hi:[0,0,1]
	v_add_f32_e32 v46, v46, v30
	v_add_f32_e32 v47, v47, v30
	v_mul_f32_e32 v30, v41, v41
	v_fmac_f32_e32 v46, v40, v40
	v_fmac_f32_e32 v47, v41, v41
	v_mul_f32_e32 v42, v28, v42
	v_mul_f32_e32 v43, v29, v43
	v_add_f32_e32 v46, v46, v30
	v_add_f32_e32 v47, v47, v30
	v_pk_fma_f32 v[42:43], v[58:59], v[20:21], v[42:43] op_sel_hi:[1,0,1] neg_lo:[0,0,1] neg_hi:[0,0,1]
	v_mul_f32_e32 v44, v28, v44
	v_mul_f32_e32 v45, v29, v45
	v_fmac_f32_e32 v46, v42, v42
	v_fmac_f32_e32 v47, v43, v43
	v_mul_f32_e32 v30, v43, v43
	v_pk_fma_f32 v[44:45], v[60:61], v[20:21], v[44:45] op_sel_hi:[1,0,1] neg_lo:[0,0,1] neg_hi:[0,0,1]
	v_add_f32_e32 v46, v46, v30
	v_add_f32_e32 v47, v47, v30
	v_mul_f32_e32 v48, v28, v64
	v_mul_f32_e32 v49, v29, v65
	v_fmac_f32_e32 v46, v44, v44
	v_fmac_f32_e32 v47, v45, v45
	v_mul_f32_e32 v30, v45, v45
	v_pk_fma_f32 v[48:49], v[2:3], v[20:21], v[48:49] op_sel_hi:[1,0,1] neg_lo:[0,0,1] neg_hi:[0,0,1]
	v_mul_f32_e32 v2, v28, v62
	v_mul_f32_e32 v3, v29, v63
	v_add_f32_e32 v46, v46, v30
	v_add_f32_e32 v47, v47, v30
	v_pk_fma_f32 v[50:51], v[0:1], v[20:21], v[2:3] op_sel_hi:[1,0,1] neg_lo:[0,0,1] neg_hi:[0,0,1]
	v_lshl_add_u64 v[14:15], v[108:109], 1, v[14:15]
	v_pk_fma_f32 v[0:1], v[50:51], v[50:51], v[46:47]
	v_mul_f32_e32 v2, v51, v51
	v_add_f32_e32 v0, v0, v2
	v_add_f32_e32 v1, v1, v2
	v_mul_f32_e32 v2, v49, v49
	v_fmac_f32_e32 v0, v48, v48
	v_fmac_f32_e32 v1, v49, v49
	s_nop 0
	v_add_f32_e32 v0, v0, v2
	v_add_f32_e32 v1, v1, v2
	v_mul_f32_e32 v2, v28, v68
	v_mul_f32_e32 v3, v29, v69
	s_nop 0
	v_pk_fma_f32 v[6:7], v[6:7], v[20:21], v[2:3] op_sel_hi:[1,0,1] neg_lo:[0,0,1] neg_hi:[0,0,1]
	v_mul_f32_e32 v2, v28, v66
	v_mul_f32_e32 v3, v29, v67
	s_nop 0
	v_pk_fma_f32 v[4:5], v[4:5], v[20:21], v[2:3] op_sel_hi:[1,0,1] neg_lo:[0,0,1] neg_hi:[0,0,1]
	s_nop 0
	v_fmac_f32_e32 v0, v4, v4
	v_fmac_f32_e32 v1, v5, v5
	v_mul_f32_e32 v2, v5, v5
	v_add_f32_e32 v0, v0, v2
	v_add_f32_e32 v1, v1, v2
	v_mul_f32_e32 v2, v7, v7
	v_fmac_f32_e32 v0, v6, v6
	v_fmac_f32_e32 v1, v7, v7
	s_nop 0
	v_add_f32_e32 v0, v0, v2
	v_add_f32_e32 v1, v1, v2
	v_mul_f32_e32 v2, v28, v72
	v_mul_f32_e32 v3, v29, v73
	s_nop 0
	v_pk_fma_f32 v[10:11], v[10:11], v[20:21], v[2:3] op_sel_hi:[1,0,1] neg_lo:[0,0,1] neg_hi:[0,0,1]
	v_mul_f32_e32 v2, v28, v70
	v_mul_f32_e32 v3, v29, v71
	s_nop 0
	v_pk_fma_f32 v[8:9], v[8:9], v[20:21], v[2:3] op_sel_hi:[1,0,1] neg_lo:[0,0,1] neg_hi:[0,0,1]
	s_nop 0
	v_fmac_f32_e32 v0, v8, v8
	v_fmac_f32_e32 v1, v9, v9
	v_mul_f32_e32 v2, v9, v9
	v_add_f32_e32 v0, v0, v2
	v_add_f32_e32 v1, v1, v2
	v_mul_f32_e32 v2, v11, v11
	v_fmac_f32_e32 v0, v10, v10
	v_fmac_f32_e32 v1, v11, v11
	s_nop 0
	v_add_f32_e32 v0, v0, v2
	v_add_f32_e32 v1, v1, v2
	v_mul_f32_e32 v2, v13, v13
	v_fmac_f32_e32 v0, v12, v12
	v_fmac_f32_e32 v1, v13, v13
	s_nop 0
	v_add_f32_e32 v0, v0, v2
	v_add_f32_e32 v1, v1, v2
	v_mul_f32_e32 v2, v17, v17
	v_fmac_f32_e32 v0, v16, v16
	v_fmac_f32_e32 v1, v17, v17
	s_nop 0
	v_add_f32_e32 v0, v0, v2
	v_add_f32_e32 v1, v1, v2
	s_nop 0
	v_mov_b32_e32 v1, v0
	s_nop 1
	v_permlane32_swap_b32_e32 v0, v1
	v_add_f32_e32 v0, v0, v1
	v_fmamk_f32 v0, v0, 0x3c800000, v246
	v_rsq_f32_e32 v20, v0
	s_nop 0
	v_mul_f32_e32 v0, v26, v20
	v_mul_f32_e32 v1, v27, v20
	v_mul_f32_e32 v2, v32, v20
	v_mul_f32_e32 v3, v33, v20
	s_waitcnt vmcnt(7)
; __device__ __forceinline__ unsigned cvt_pk_bf16(float lo, float hi) { f32x2 v = {lo, hi}; bf16x2_t b = __builtin_convertvector(v, bf16x2_t); return __builtin_bit_cast(unsigned, b); }
; __device__ __forceinline__ float swapsum(float a) { auto rr = __builtin_amdgcn_permlane32_swap(__float_as_uint(a), __float_as_uint(a), false, false); return __uint_as_float(rr[0]) + __uint_as_float(rr[1]); }
;     ...
;             const float rs = __builtin_amdgcn_rsqf(swapsum(ss) * (1.f / 64.f) + 1e-6f);
;             bf16_t* op = (bf16_t*)outp + (size_t)qidx * opitch + 4 * hf;
; #pragma unroll
;             for (int db = 0; db < 2; ++db)
; #pragma unroll
;                 for (int g = 0; g < 4; ++g) { const f32x4 gn = *(const f32x4*)(gain + 32 * db + 8 * g + 4 * hf); const int i0 = 16 * db + 4 * g;
;                     *(u32x2*)(op + 32 * db + 8 * g) = (u32x2){cvt_pk_bf16(o[i0] * rs * gn[0], o[i0 + 1] * rs * gn[1]), cvt_pk_bf16(o[i0 + 2] * rs * gn[2], o[i0 + 3] * rs * gn[3])}; }
	v_mul_f32_e32 v0, v212, v0
	v_mul_f32_e32 v1, v213, v1
	v_mul_f32_e32 v2, v214, v2
	v_mul_f32_e32 v3, v215, v3
	v_cvt_pk_bf16_f32 v212, v0, v1
	v_cvt_pk_bf16_f32 v213, v2, v3
	v_mul_f32_e32 v22, v34, v20
	v_mul_f32_e32 v23, v35, v20
	v_mul_f32_e32 v4, v4, v20
	v_mul_f32_e32 v5, v5, v20
	s_waitcnt vmcnt(6)
	v_mul_f32_e32 v0, v216, v22
	v_mul_f32_e32 v1, v217, v23
	v_mul_f32_e32 v22, v36, v20
	v_mul_f32_e32 v23, v37, v20
	v_cvt_pk_bf16_f32 v216, v0, v1
	v_mul_f32_e32 v2, v218, v22
	v_mul_f32_e32 v3, v219, v23
	v_mul_f32_e32 v22, v38, v20
	v_mul_f32_e32 v23, v39, v20
	v_cvt_pk_bf16_f32 v217, v2, v3
	s_waitcnt vmcnt(5)
	v_mul_f32_e32 v0, v220, v22
	v_mul_f32_e32 v1, v221, v23
	v_mul_f32_e32 v22, v40, v20
	v_mul_f32_e32 v23, v41, v20
	v_cvt_pk_bf16_f32 v220, v0, v1
	v_mul_f32_e32 v2, v222, v22
	v_mul_f32_e32 v3, v223, v23
	v_mul_f32_e32 v22, v42, v20
	v_mul_f32_e32 v23, v43, v20
	v_cvt_pk_bf16_f32 v221, v2, v3
	s_waitcnt vmcnt(4)
	v_mul_f32_e32 v0, v22, v224
	v_mul_f32_e32 v1, v23, v225
	v_mul_f32_e32 v22, v44, v20
	v_mul_f32_e32 v23, v45, v20
	v_cvt_pk_bf16_f32 v224, v0, v1
	v_mul_f32_e32 v2, v22, v226
	v_mul_f32_e32 v3, v23, v227
	v_mul_f32_e32 v22, v50, v20
	v_mul_f32_e32 v23, v51, v20
	v_cvt_pk_bf16_f32 v225, v2, v3
	s_waitcnt vmcnt(3)
	v_mul_f32_e32 v0, v22, v228
	v_mul_f32_e32 v1, v23, v229
	v_mul_f32_e32 v22, v48, v20
	v_mul_f32_e32 v23, v49, v20
	v_cvt_pk_bf16_f32 v214, v0, v1
	v_mul_f32_e32 v2, v22, v230
	v_mul_f32_e32 v3, v23, v231
	s_nop 0
	v_cvt_pk_bf16_f32 v215, v2, v3
	s_waitcnt vmcnt(2)
	v_mul_f32_e32 v0, v4, v232
	v_mul_f32_e32 v1, v5, v233
	v_mul_f32_e32 v4, v6, v20
	v_mul_f32_e32 v5, v7, v20
	v_cvt_pk_bf16_f32 v218, v0, v1
	v_mul_f32_e32 v2, v4, v234
	v_mul_f32_e32 v3, v5, v235
	v_mul_f32_e32 v4, v8, v20
	v_mul_f32_e32 v5, v9, v20
	v_cvt_pk_bf16_f32 v219, v2, v3
	s_waitcnt vmcnt(1)
	v_mul_f32_e32 v0, v4, v236
	v_mul_f32_e32 v1, v5, v237
	v_mul_f32_e32 v4, v10, v20
	v_mul_f32_e32 v5, v11, v20
	v_cvt_pk_bf16_f32 v222, v0, v1
	v_mul_f32_e32 v2, v4, v238
	v_mul_f32_e32 v3, v5, v239
	v_mul_f32_e32 v4, v12, v20
	v_mul_f32_e32 v5, v13, v20
	v_cvt_pk_bf16_f32 v223, v2, v3
	s_waitcnt vmcnt(0)
	v_mul_f32_e32 v0, v4, v240
	v_mul_f32_e32 v1, v5, v241
	v_mul_f32_e32 v4, v16, v20
	v_mul_f32_e32 v5, v17, v20
	v_cvt_pk_bf16_f32 v226, v0, v1
	v_mul_f32_e32 v2, v4, v242
	v_mul_f32_e32 v3, v5, v243
	s_nop 0
	v_cvt_pk_bf16_f32 v227, v2, v3
	s_nop 1
	v_permlane32_swap_b32_e32 v212, v214
	v_permlane32_swap_b32_e32 v213, v215
	v_permlane32_swap_b32_e32 v216, v218
	v_permlane32_swap_b32_e32 v217, v219
	v_permlane32_swap_b32_e32 v220, v222
	v_permlane32_swap_b32_e32 v221, v223
	v_permlane32_swap_b32_e32 v224, v226
	v_permlane32_swap_b32_e32 v225, v227
	v_mbcnt_lo_u32_b32 v22, -1, 0
	v_mbcnt_hi_u32_b32 v22, -1, v22
	v_lshrrev_b32_e32 v22, 5, v22
	v_mul_u32_u24_e32 v22, 56, v22
	v_mov_b32_e32 v23, 0
	v_lshl_add_u64 v[14:15], v[22:23], 0, v[14:15]
	global_store_dwordx4 v[14:15], v[212:215], off offset:2048
	global_store_dwordx4 v[14:15], v[216:219], off offset:2064
	global_store_dwordx4 v[14:15], v[220:223], off offset:2080
	global_store_dwordx4 v[14:15], v[224:227], off offset:2096
	s_branch .LBB0_918

; #define LAS __attribute__((address_space(3)))
; __device__ __forceinline__ void sb_unit(LAS unsigned char* lds, int wv, int lane, const Tens T, int q0, bf16_t* outp, int opitch, unsigned* nctr, int* pend) {
;     ...
;         if (!done && k0 <= qmax) {
;             LAS unsigned char* kb = lds + (buf ? KB1 : KB0) + r32 * KS + hf * 16;
;             f32x16 st[2]; bf16x8 kfr[2][4];
; #pragma unroll
;             for (int kk = 0; kk < 2; ++kk)
; #pragma unroll
;                 for (int c = 0; c < 4; ++c) kfr[kk][c] = *(const LAS bf16x8*)(kb + kk * 32 * KS + c * 32);
; #pragma unroll
;             for (int kk = 0; kk < 2; ++kk)
; #pragma unroll
;                 for (int i = 0; i < 16; ++i) st[kk][i] = 0.f;
;             __builtin_amdgcn_sched_barrier(0);
; #pragma unroll
;             for (int c = 0; c < 4; ++c)
; #pragma unroll
;                 for (int kk = 0; kk < 2; ++kk) st[kk] = __builtin_amdgcn_mfma_f32_32x32x16_bf16(kfr[kk][c], qf[c], st[kk], 0, 0, 0);
;             __builtin_amdgcn_sched_barrier(0);
;             float lb[2][16], l1[2][16];
; #pragma unroll
;             for (int kk = 0; kk < 2; ++kk)
; #pragma unroll
;                 for (int i = 0; i < 16; ++i) { const float z = st[kk][i]; const int key = k0 + 32 * kk + 8 * (i >> 2) + 4 * hf + (i & 3);
;                     const float lg = __builtin_amdgcn_logf(1.f + __builtin_amdgcn_exp2f(-fabsf(z)));
;                     const float b = fminf(z, 0.f) - lg; const bool valid = key < qidx;
;                     lb[kk][i] = valid ? b : -INFINITY; l1[kk][i] = valid ? b - z : 0.f; }
.LBB0_1007:
	s_xor_b64 s[16:17], s[16:17], -1
	s_andn2_b64 vcc, exec, s[16:17]
	s_mov_b64 s[16:17], -1
	s_cbranch_vccnz .LBB0_1010
	s_cmp_gt_i32 s28, s21
	s_mov_b64 s[16:17], 0
	s_cbranch_scc1 .LBB0_1010
	s_cmp_eq_u32 s29, 0
	s_cselect_b32 s16, 0, 0x3400
	v_add_u32_e32 v52, s16, v93
	ds_read_b128 v[48:51], v52
	ds_read_b128 v[100:103], v52 offset:32
	ds_read_b128 v[104:107], v52 offset:64
	ds_read_b128 v[108:111], v52 offset:96
	ds_read_b128 v[64:67], v52 offset:4608
	ds_read_b128 v[112:115], v52 offset:4640
	ds_read_b128 v[116:119], v52 offset:4672
	ds_read_b128 v[120:123], v52 offset:4704
	s_waitcnt lgkmcnt(7)
	v_mfma_f32_32x32x16_bf16 v[48:63], v[48:51], v[16:19], 0
	s_waitcnt lgkmcnt(3)
	v_mfma_f32_32x32x16_bf16 v[64:79], v[64:67], v[16:19], 0
	v_mfma_f32_32x32x16_bf16 v[48:63], v[100:103], v[20:23], v[48:63]
	s_waitcnt lgkmcnt(2)
	v_mfma_f32_32x32x16_bf16 v[64:79], v[112:115], v[20:23], v[64:79]
	v_mfma_f32_32x32x16_bf16 v[48:63], v[104:107], v[24:27], v[48:63]
	s_waitcnt lgkmcnt(1)
	v_mfma_f32_32x32x16_bf16 v[64:79], v[116:119], v[24:27], v[64:79]
	v_mfma_f32_32x32x16_bf16 v[48:63], v[108:111], v[80:83], v[48:63]
	s_waitcnt lgkmcnt(0)
	v_mfma_f32_32x32x16_bf16 v[64:79], v[120:123], v[80:83], v[64:79]
	s_nop 9
	v_exp_f32_e64 v99, -|v48|
	v_exp_f32_e64 v101, -|v49|
	v_max_f32_e32 v100, v48, v48
	v_min_f32_e32 v106, 0, v100
	v_add_f32_e32 v99, 1.0, v99
	v_log_f32_e32 v104, v99
	v_add_f32_e32 v99, 1.0, v101
	v_log_f32_e32 v100, v99
	v_exp_f32_e64 v99, -|v50|
	v_max_f32_e32 v101, v49, v49
	v_min_f32_e32 v102, 0, v101
	v_exp_f32_e64 v101, -|v51|
	v_add_f32_e32 v99, 1.0, v99
	v_exp_f32_e64 v108, -|v52|
	v_log_f32_e32 v105, v99
	v_max_f32_e32 v99, v50, v50
	v_min_f32_e32 v107, 0, v99
	v_add_f32_e32 v99, 1.0, v101
	v_log_f32_e32 v101, v99
	v_max_f32_e32 v99, v51, v51
	v_min_f32_e32 v103, 0, v99
	v_add_f32_e32 v99, 1.0, v108
	v_exp_f32_e64 v108, -|v53|
	v_exp_f32_e64 v109, -|v54|
	v_log_f32_e32 v112, v99
	v_max_f32_e32 v99, v52, v52
	v_min_f32_e32 v114, 0, v99
	v_add_f32_e32 v99, 1.0, v108
	v_log_f32_e32 v108, v99
	v_max_f32_e32 v99, v53, v53
	v_min_f32_e32 v110, 0, v99
	v_add_f32_e32 v99, 1.0, v109
	v_exp_f32_e64 v109, -|v55|
	v_exp_f32_e64 v116, -|v56|
	v_log_f32_e32 v113, v99
	v_max_f32_e32 v99, v54, v54
	v_min_f32_e32 v115, 0, v99
	v_add_f32_e32 v99, 1.0, v109
	v_log_f32_e32 v109, v99
	v_max_f32_e32 v99, v55, v55
	v_min_f32_e32 v111, 0, v99
	v_add_f32_e32 v99, 1.0, v116
	v_exp_f32_e64 v116, -|v57|
	v_exp_f32_e64 v117, -|v58|
	v_log_f32_e32 v120, v99
	v_max_f32_e32 v99, v56, v56
	v_min_f32_e32 v122, 0, v99
	v_add_f32_e32 v99, 1.0, v116
	v_log_f32_e32 v116, v99
	v_max_f32_e32 v99, v57, v57
	v_min_f32_e32 v118, 0, v99
	v_add_f32_e32 v99, 1.0, v117
	v_exp_f32_e64 v117, -|v59|
	v_exp_f32_e64 v124, -|v60|
	v_log_f32_e32 v121, v99
	v_max_f32_e32 v99, v58, v58
	v_min_f32_e32 v123, 0, v99
	v_add_f32_e32 v99, 1.0, v117
	v_log_f32_e32 v117, v99
	v_max_f32_e32 v99, v59, v59
	v_min_f32_e32 v119, 0, v99
	v_add_f32_e32 v99, 1.0, v124
	v_exp_f32_e64 v124, -|v61|
	v_exp_f32_e64 v125, -|v62|
	v_log_f32_e32 v128, v99
	v_max_f32_e32 v99, v60, v60
	v_min_f32_e32 v130, 0, v99
	v_add_f32_e32 v99, 1.0, v124
	v_log_f32_e32 v124, v99
	v_max_f32_e32 v99, v61, v61
	v_min_f32_e32 v126, 0, v99
	v_add_f32_e32 v99, 1.0, v125
	v_exp_f32_e64 v125, -|v63|
	v_exp_f32_e64 v132, -|v64|
	v_log_f32_e32 v129, v99
	v_max_f32_e32 v99, v62, v62
	v_min_f32_e32 v131, 0, v99
	v_add_f32_e32 v99, 1.0, v125
	v_log_f32_e32 v125, v99
	v_max_f32_e32 v99, v63, v63
	v_min_f32_e32 v127, 0, v99
	v_add_f32_e32 v99, 1.0, v132
	v_exp_f32_e64 v132, -|v65|
	v_exp_f32_e64 v133, -|v66|
	v_log_f32_e32 v136, v99
	v_max_f32_e32 v99, v64, v64
	v_min_f32_e32 v138, 0, v99
	v_add_f32_e32 v99, 1.0, v132
	v_log_f32_e32 v132, v99
	v_max_f32_e32 v99, v65, v65
	v_min_f32_e32 v134, 0, v99
	v_add_f32_e32 v99, 1.0, v133
	v_exp_f32_e64 v133, -|v67|
	v_exp_f32_e64 v145, -|v68|
	v_log_f32_e32 v137, v99
	v_max_f32_e32 v99, v66, v66
	v_min_f32_e32 v139, 0, v99
	v_add_f32_e32 v99, 1.0, v133
	v_log_f32_e32 v133, v99
	v_max_f32_e32 v99, v67, v67
	v_min_f32_e32 v135, 0, v99
	v_add_f32_e32 v99, 1.0, v145
	v_exp_f32_e64 v145, -|v69|
	v_log_f32_e32 v146, v99
	v_max_f32_e32 v99, v68, v68
	v_min_f32_e32 v148, 0, v99
	v_add_f32_e32 v99, 1.0, v145
	v_exp_f32_e64 v145, -|v70|
	v_log_f32_e32 v150, v99
	v_max_f32_e32 v99, v69, v69
	v_min_f32_e32 v152, 0, v99
	v_add_f32_e32 v99, 1.0, v145
	v_exp_f32_e64 v145, -|v71|
	v_log_f32_e32 v147, v99
	v_max_f32_e32 v99, v70, v70
	v_min_f32_e32 v149, 0, v99
	v_add_f32_e32 v99, 1.0, v145
	v_exp_f32_e64 v145, -|v72|
	v_log_f32_e32 v151, v99
	v_max_f32_e32 v99, v71, v71
	v_min_f32_e32 v153, 0, v99
	v_add_f32_e32 v99, 1.0, v145
	v_exp_f32_e64 v145, -|v73|
	v_log_f32_e32 v154, v99
	v_max_f32_e32 v99, v72, v72
	v_min_f32_e32 v156, 0, v99
	v_add_f32_e32 v99, 1.0, v145
	v_exp_f32_e64 v145, -|v74|
	v_log_f32_e32 v158, v99
	v_max_f32_e32 v99, v73, v73
	v_min_f32_e32 v160, 0, v99
	v_add_f32_e32 v99, 1.0, v145
	v_exp_f32_e64 v145, -|v75|
	v_log_f32_e32 v155, v99
	v_max_f32_e32 v99, v74, v74
	v_min_f32_e32 v157, 0, v99
	v_add_f32_e32 v99, 1.0, v145
	v_exp_f32_e64 v145, -|v76|
	v_log_f32_e32 v159, v99
	v_max_f32_e32 v99, v75, v75
	v_min_f32_e32 v161, 0, v99
	v_add_f32_e32 v99, 1.0, v145
	v_exp_f32_e64 v145, -|v77|
	v_log_f32_e32 v162, v99
	v_max_f32_e32 v99, v76, v76
	v_min_f32_e32 v166, 0, v99
	v_add_f32_e32 v99, 1.0, v145
	v_exp_f32_e64 v145, -|v78|
	v_log_f32_e32 v168, v99
	v_max_f32_e32 v99, v77, v77
	v_min_f32_e32 v170, 0, v99
	v_add_f32_e32 v99, 1.0, v145
	v_exp_f32_e64 v145, -|v79|
	v_log_f32_e32 v163, v99
	v_max_f32_e32 v99, v78, v78
	v_min_f32_e32 v167, 0, v99
	v_add_f32_e32 v99, 1.0, v145
; __device__ __forceinline__ unsigned cvt_pk_bf16(float lo, float hi) { f32x2 v = {lo, hi}; bf16x2_t b = __builtin_convertvector(v, bf16x2_t); return __builtin_bit_cast(unsigned, b); }
; __device__ __forceinline__ void sb_unit(LAS unsigned char* lds, int wv, int lane, const Tens T, int q0, bf16_t* outp, int opitch, unsigned* nctr, int* pend) {
;     ...
;                 for (int i = 0; i < 16; ++i) { const float z = st[kk][i]; const int key = k0 + 32 * kk + 8 * (i >> 2) + 4 * hf + (i & 3);
;                     const float lg = __builtin_amdgcn_logf(1.f + __builtin_amdgcn_exp2f(-fabsf(z)));
;                     const float b = fminf(z, 0.f) - lg; const bool valid = key < qidx;
;                     lb[kk][i] = valid ? b : -INFINITY; l1[kk][i] = valid ? b - z : 0.f; }
;             float P = R; unsigned pk[2][8];
; #pragma unroll
;     ...
; #pragma unroll
;                 for (int g = 3; g >= 0; --g) {
;                     const float G = (l1[kk][4 * g] + l1[kk][4 * g + 1]) + (l1[kk][4 * g + 2] + l1[kk][4 * g + 3]);
;                     auto rr = __builtin_amdgcn_permlane32_swap(__float_as_uint(G), __float_as_uint(G), false, false);
;                     const float G0 = __uint_as_float(rr[0]), G1 = __uint_as_float(rr[1]);
;                     const float pre = P + (hf == 0 ? G1 : 0.f);
;                     const float s3 = pre, s2 = s3 + l1[kk][4 * g + 3], s1 = s2 + l1[kk][4 * g + 2], s0 = s1 + l1[kk][4 * g + 1];
;                     const float a0 = __builtin_amdgcn_exp2f(lb[kk][4 * g] + s0), a1 = __builtin_amdgcn_exp2f(lb[kk][4 * g + 1] + s1), a2 = __builtin_amdgcn_exp2f(lb[kk][4 * g + 2] + s2), a3 = __builtin_amdgcn_exp2f(lb[kk][4 * g + 3] + s3);
;                     pk[kk][2 * g] = cvt_pk_bf16(a0, a1); pk[kk][2 * g + 1] = cvt_pk_bf16(a2, a3);
;                     P += G0 + G1;
;                 }
	v_log_f32_e32 v169, v99
	v_add_u32_e32 v143, s28, v30
	v_max_f32_e32 v99, v79, v79
	v_min_f32_e32 v171, 0, v99
	v_add_u32_e32 v99, 56, v143
	v_add_u32_e32 v145, 58, v143
	v_sub_f32_e32 v162, v166, v162
	v_sub_f32_e32 v163, v167, v163
	v_cmp_lt_i32_e32 vcc, v99, v28
	v_sub_f32_e32 v166, v170, v168
	v_sub_f32_e32 v167, v171, v169
	v_cmp_lt_i32_e64 s[48:49], v145, v29
	v_mov_b32_e32 v168, v76
	v_mov_b32_e32 v169, v78
	v_cndmask_b32_e32 v99, v200, v162, vcc
	v_add_u32_e32 v165, 57, v143
	v_add_u32_e32 v172, 59, v143
	v_cndmask_b32_e64 v145, v200, v163, s[48:49]
	v_sub_f32_e32 v162, v162, v168
	v_sub_f32_e32 v163, v163, v169
	v_mov_b32_e32 v78, v77
	v_cmp_lt_i32_e64 s[46:47], v165, v28
	v_cndmask_b32_e32 v162, 0, v162, vcc
	v_cmp_lt_i32_e32 vcc, v172, v29
	v_sub_f32_e32 v76, v166, v78
	v_sub_f32_e32 v77, v167, v79
	v_cndmask_b32_e64 v163, 0, v163, s[48:49]
	v_cndmask_b32_e32 v77, 0, v77, vcc
	v_cndmask_b32_e64 v76, 0, v76, s[46:47]
	v_add_f32_e32 v78, v162, v76
	v_add_f32_e32 v79, v163, v77
	v_cndmask_b32_e64 v165, v200, v166, s[46:47]
	v_pk_add_f32 v[78:79], v[78:79], v[78:79] op_sel:[0,1] op_sel_hi:[1,0]
	v_cndmask_b32_e32 v168, v200, v167, vcc
	v_mov_b32_e32 v79, v78
	s_nop 1
	v_permlane32_swap_b32_e32 v78, v79
	v_cndmask_b32_e64 v162, 0, v79, s[42:43]
	v_add_f32_e32 v162, v98, v162
	v_add_f32_e32 v77, v162, v77
	v_add_f32_e32 v163, v163, v77
	v_add_f32_e32 v76, v76, v163
	v_add_f32_e32 v76, v99, v76
	v_exp_f32_e32 v166, v76
	v_add_f32_e32 v76, v165, v163
	v_exp_f32_e32 v163, v76
	v_add_f32_e32 v76, v145, v77
	v_exp_f32_e32 v145, v76
	v_add_f32_e32 v76, v162, v168
	v_add_u32_e32 v77, 48, v143
	v_add_u32_e32 v99, 50, v143
	v_exp_f32_e32 v162, v76
	v_add_f32_e32 v76, v78, v79
	v_sub_f32_e32 v78, v156, v154
	v_sub_f32_e32 v79, v157, v155
	v_cmp_lt_i32_e32 vcc, v77, v28
	v_cmp_lt_i32_e64 s[48:49], v99, v29
	v_mov_b32_e32 v156, v72
	v_mov_b32_e32 v157, v74
	v_cndmask_b32_e32 v165, v200, v78, vcc
	v_add_u32_e32 v77, 49, v143
	v_add_u32_e32 v167, 51, v143
	v_sub_f32_e32 v154, v160, v158
	v_sub_f32_e32 v155, v161, v159
	v_cndmask_b32_e64 v159, v200, v79, s[48:49]
	v_sub_f32_e32 v78, v78, v156
	v_sub_f32_e32 v79, v79, v157
	v_mov_b32_e32 v74, v73
	v_cmp_lt_i32_e64 s[46:47], v77, v28
	v_cndmask_b32_e32 v78, 0, v78, vcc
	v_cmp_lt_i32_e32 vcc, v167, v29
	v_sub_f32_e32 v72, v154, v74
	v_sub_f32_e32 v73, v155, v75
	v_cndmask_b32_e64 v79, 0, v79, s[48:49]
	v_cndmask_b32_e32 v73, 0, v73, vcc
	v_cndmask_b32_e64 v72, 0, v72, s[46:47]
	v_add_f32_e32 v74, v78, v72
	v_add_f32_e32 v75, v79, v73
	v_cndmask_b32_e64 v158, v200, v154, s[46:47]
	v_pk_add_f32 v[74:75], v[74:75], v[74:75] op_sel:[0,1] op_sel_hi:[1,0]
	v_cndmask_b32_e32 v156, v200, v155, vcc
	v_mov_b32_e32 v77, v74
	s_nop 1
	v_permlane32_swap_b32_e32 v74, v77
	v_mov_b32_e32 v99, v74
	v_cndmask_b32_e64 v75, 0, v77, s[42:43]
	v_add_f32_e32 v76, v98, v76
	v_add_f32_e32 v77, v99, v77
	v_sub_f32_e32 v98, v152, v150
	v_sub_f32_e32 v99, v153, v151
	v_add_f32_e32 v74, v76, v75
	v_add_f32_e32 v73, v74, v73
	v_add_f32_e32 v75, v79, v73
	v_add_f32_e32 v72, v72, v75
	v_add_f32_e32 v72, v165, v72
	v_add_f32_e32 v75, v158, v75
	v_add_f32_e32 v73, v159, v73
	v_add_f32_e32 v74, v156, v74
	v_exp_f32_e32 v72, v72
	v_exp_f32_e32 v78, v75
	v_exp_f32_e32 v73, v73
	v_exp_f32_e32 v79, v74
	v_pk_add_f32 v[76:77], v[76:77], v[76:77] op_sel:[0,1] op_sel_hi:[1,0]
	v_cvt_pk_bf16_f32 v75, v145, v162
	v_cvt_pk_bf16_f32 v72, v72, v78
	v_cvt_pk_bf16_f32 v73, v73, v79
	v_add_u32_e32 v77, 40, v143
	v_add_u32_e32 v145, 42, v143
	v_sub_f32_e32 v78, v148, v146
	v_sub_f32_e32 v79, v149, v147
	v_add_u32_e32 v146, 41, v143
	v_cmp_lt_i32_e32 vcc, v77, v28
	v_cmp_lt_i32_e64 s[46:47], v146, v28
	v_cmp_lt_i32_e64 s[48:49], v145, v29
	v_mov_b32_e32 v146, v68
	v_mov_b32_e32 v147, v70
	v_cndmask_b32_e32 v77, v200, v78, vcc
	v_add_u32_e32 v148, 43, v143
	v_cndmask_b32_e64 v145, v200, v79, s[48:49]
	v_sub_f32_e32 v78, v78, v146
	v_sub_f32_e32 v79, v79, v147
	v_mov_b32_e32 v70, v69
	v_cndmask_b32_e32 v78, 0, v78, vcc
	v_cmp_lt_i32_e32 vcc, v148, v29
	v_sub_f32_e32 v68, v98, v70
	v_sub_f32_e32 v69, v99, v71
	v_cndmask_b32_e64 v79, 0, v79, s[48:49]
	v_cndmask_b32_e32 v69, 0, v69, vcc
	v_cndmask_b32_e64 v68, 0, v68, s[46:47]
	v_add_f32_e32 v70, v78, v68
	v_add_f32_e32 v71, v79, v69
	v_cndmask_b32_e64 v149, v200, v98, s[46:47]
	v_pk_add_f32 v[70:71], v[70:71], v[70:71] op_sel:[0,1] op_sel_hi:[1,0]
	v_cndmask_b32_e32 v146, v200, v99, vcc
	v_mov_b32_e32 v71, v70
	s_nop 1
	v_permlane32_swap_b32_e32 v70, v71
	v_cndmask_b32_e64 v78, 0, v71, s[42:43]
	v_add_f32_e32 v78, v76, v78
	v_add_f32_e32 v69, v69, v78
	v_add_f32_e32 v79, v79, v69
	v_add_f32_e32 v68, v68, v79
	v_add_f32_e32 v68, v77, v68
	v_exp_f32_e32 v147, v68
	v_add_f32_e32 v68, v149, v79
	v_exp_f32_e32 v148, v68
	v_add_f32_e32 v68, v145, v69
	v_exp_f32_e32 v145, v68
	v_add_f32_e32 v68, v146, v78
	v_add_u32_e32 v69, 32, v143
	v_add_u32_e32 v77, 34, v143
	v_exp_f32_e32 v146, v68
	v_add_f32_e32 v68, v70, v71
	v_sub_f32_e32 v70, v138, v136
	v_sub_f32_e32 v71, v139, v137
	v_cmp_lt_i32_e32 vcc, v69, v28
	v_cmp_lt_i32_e64 s[48:49], v77, v29
	v_mov_b32_e32 v98, v64
	v_mov_b32_e32 v99, v66
	v_cndmask_b32_e32 v136, v200, v70, vcc
	v_or_b32_e32 v137, 3, v69
	v_or_b32_e32 v69, 1, v69
	v_sub_f32_e32 v78, v134, v132
	v_sub_f32_e32 v79, v135, v133
	v_cndmask_b32_e64 v133, v200, v71, s[48:49]
	v_sub_f32_e32 v70, v70, v98
	v_sub_f32_e32 v71, v71, v99
	v_mov_b32_e32 v66, v65
	v_cmp_lt_i32_e64 s[46:47], v69, v28
	v_cndmask_b32_e32 v70, 0, v70, vcc
	v_cmp_lt_i32_e32 vcc, v137, v29
	v_sub_f32_e32 v64, v78, v66
	v_sub_f32_e32 v65, v79, v67
	v_cndmask_b32_e64 v71, 0, v71, s[48:49]
	v_cndmask_b32_e32 v65, 0, v65, vcc
; __device__ __forceinline__ unsigned cvt_pk_bf16(float lo, float hi) { f32x2 v = {lo, hi}; bf16x2_t b = __builtin_convertvector(v, bf16x2_t); return __builtin_bit_cast(unsigned, b); }
; __device__ __forceinline__ void sb_unit(LAS unsigned char* lds, int wv, int lane, const Tens T, int q0, bf16_t* outp, int opitch, unsigned* nctr, int* pend) {
;     ...
;                 for (int i = 0; i < 16; ++i) { const float z = st[kk][i]; const int key = k0 + 32 * kk + 8 * (i >> 2) + 4 * hf + (i & 3);
;                     const float lg = __builtin_amdgcn_logf(1.f + __builtin_amdgcn_exp2f(-fabsf(z)));
;                     const float b = fminf(z, 0.f) - lg; const bool valid = key < qidx;
;                     lb[kk][i] = valid ? b : -INFINITY; l1[kk][i] = valid ? b - z : 0.f; }
;             float P = R; unsigned pk[2][8];
; #pragma unroll
;     ...
; #pragma unroll
;                 for (int g = 3; g >= 0; --g) {
;                     const float G = (l1[kk][4 * g] + l1[kk][4 * g + 1]) + (l1[kk][4 * g + 2] + l1[kk][4 * g + 3]);
;                     auto rr = __builtin_amdgcn_permlane32_swap(__float_as_uint(G), __float_as_uint(G), false, false);
;                     const float G0 = __uint_as_float(rr[0]), G1 = __uint_as_float(rr[1]);
;                     const float pre = P + (hf == 0 ? G1 : 0.f);
;                     const float s3 = pre, s2 = s3 + l1[kk][4 * g + 3], s1 = s2 + l1[kk][4 * g + 2], s0 = s1 + l1[kk][4 * g + 1];
;                     const float a0 = __builtin_amdgcn_exp2f(lb[kk][4 * g] + s0), a1 = __builtin_amdgcn_exp2f(lb[kk][4 * g + 1] + s1), a2 = __builtin_amdgcn_exp2f(lb[kk][4 * g + 2] + s2), a3 = __builtin_amdgcn_exp2f(lb[kk][4 * g + 3] + s3);
;                     pk[kk][2 * g] = cvt_pk_bf16(a0, a1); pk[kk][2 * g + 1] = cvt_pk_bf16(a2, a3);
;                     P += G0 + G1;
;                 }
	v_cndmask_b32_e64 v64, 0, v64, s[46:47]
	v_add_f32_e32 v66, v70, v64
	v_add_f32_e32 v67, v71, v65
	v_cndmask_b32_e64 v132, v200, v78, s[46:47]
	v_pk_add_f32 v[66:67], v[66:67], v[66:67] op_sel:[0,1] op_sel_hi:[1,0]
	v_cndmask_b32_e32 v98, v200, v79, vcc
	v_mov_b32_e32 v69, v66
	s_nop 1
	v_permlane32_swap_b32_e32 v66, v69
	v_mov_b32_e32 v77, v66
	v_cndmask_b32_e64 v67, 0, v69, s[42:43]
	v_add_f32_e32 v68, v76, v68
	v_add_f32_e32 v69, v77, v69
	v_add_u32_e32 v78, 26, v143
	v_add_f32_e32 v66, v68, v67
	v_add_f32_e32 v65, v65, v66
	v_add_f32_e32 v67, v71, v65
	v_add_f32_e32 v64, v64, v67
	v_add_f32_e32 v64, v136, v64
	v_add_f32_e32 v67, v132, v67
	v_add_f32_e32 v65, v133, v65
	v_add_f32_e32 v66, v98, v66
	v_exp_f32_e32 v64, v64
	v_exp_f32_e32 v70, v67
	v_exp_f32_e32 v65, v65
	v_exp_f32_e32 v71, v66
	v_pk_add_f32 v[68:69], v[68:69], v[68:69] op_sel:[0,1] op_sel_hi:[1,0]
	v_add_u32_e32 v79, 25, v143
	v_add_u32_e32 v69, 24, v143
	v_cvt_pk_bf16_f32 v64, v64, v70
	v_cvt_pk_bf16_f32 v65, v65, v71
	v_sub_f32_e32 v70, v130, v128
	v_sub_f32_e32 v71, v131, v129
	v_cmp_lt_i32_e32 vcc, v69, v28
	v_cmp_lt_i32_e64 s[46:47], v79, v28
	v_cmp_lt_i32_e64 s[48:49], v78, v29
	v_mov_b32_e32 v78, v60
	v_mov_b32_e32 v79, v62
	v_cndmask_b32_e32 v69, v200, v70, vcc
	v_add_u32_e32 v98, 27, v143
	v_sub_f32_e32 v76, v126, v124
	v_sub_f32_e32 v77, v127, v125
	v_cndmask_b32_e64 v124, v200, v71, s[48:49]
	v_sub_f32_e32 v70, v70, v78
	v_sub_f32_e32 v71, v71, v79
	v_mov_b32_e32 v62, v61
	v_cndmask_b32_e32 v70, 0, v70, vcc
	v_cmp_lt_i32_e32 vcc, v98, v29
	v_sub_f32_e32 v60, v76, v62
	v_sub_f32_e32 v61, v77, v63
	v_cndmask_b32_e64 v71, 0, v71, s[48:49]
	v_cndmask_b32_e32 v61, 0, v61, vcc
	v_cndmask_b32_e64 v60, 0, v60, s[46:47]
	v_add_f32_e32 v62, v70, v60
	v_add_f32_e32 v63, v71, v61
	v_cndmask_b32_e64 v99, v200, v76, s[46:47]
	v_pk_add_f32 v[62:63], v[62:63], v[62:63] op_sel:[0,1] op_sel_hi:[1,0]
	v_cndmask_b32_e32 v78, v200, v77, vcc
	v_mov_b32_e32 v63, v62
	s_nop 1
	v_permlane32_swap_b32_e32 v62, v63
	v_cndmask_b32_e64 v70, 0, v63, s[42:43]
	v_add_f32_e32 v70, v68, v70
	v_add_f32_e32 v61, v61, v70
	v_add_f32_e32 v71, v71, v61
	v_add_f32_e32 v60, v60, v71
	v_add_f32_e32 v60, v69, v60
	v_exp_f32_e32 v79, v60
	v_add_f32_e32 v60, v99, v71
	v_exp_f32_e32 v98, v60
	v_add_f32_e32 v60, v124, v61
	v_exp_f32_e32 v99, v60
	v_add_f32_e32 v60, v78, v70
	v_add_u32_e32 v61, 16, v143
	v_add_u32_e32 v69, 18, v143
	v_exp_f32_e32 v78, v60
	v_add_f32_e32 v60, v62, v63
	v_sub_f32_e32 v62, v122, v120
	v_sub_f32_e32 v63, v123, v121
	v_cmp_lt_i32_e32 vcc, v61, v28
	v_cmp_lt_i32_e64 s[48:49], v69, v29
	v_mov_b32_e32 v76, v56
	v_mov_b32_e32 v77, v58
	v_cndmask_b32_e32 v120, v200, v62, vcc
	v_add_u32_e32 v61, 17, v143
	v_add_u32_e32 v121, 19, v143
	v_sub_f32_e32 v70, v118, v116
	v_sub_f32_e32 v71, v119, v117
	v_cndmask_b32_e64 v117, v200, v63, s[48:49]
	v_sub_f32_e32 v62, v62, v76
	v_sub_f32_e32 v63, v63, v77
	v_mov_b32_e32 v58, v57
	v_cmp_lt_i32_e64 s[46:47], v61, v28
	v_cndmask_b32_e32 v62, 0, v62, vcc
	v_cmp_lt_i32_e32 vcc, v121, v29
	v_sub_f32_e32 v56, v70, v58
	v_sub_f32_e32 v57, v71, v59
	v_cndmask_b32_e64 v63, 0, v63, s[48:49]
	v_cndmask_b32_e32 v57, 0, v57, vcc
	v_cndmask_b32_e64 v56, 0, v56, s[46:47]
	v_add_f32_e32 v58, v62, v56
	v_add_f32_e32 v59, v63, v57
	v_cndmask_b32_e64 v116, v200, v70, s[46:47]
	v_pk_add_f32 v[58:59], v[58:59], v[58:59] op_sel:[0,1] op_sel_hi:[1,0]
	v_cndmask_b32_e32 v76, v200, v71, vcc
	v_mov_b32_e32 v61, v58
	s_nop 1
	v_permlane32_swap_b32_e32 v58, v61
	v_mov_b32_e32 v69, v58
	v_cndmask_b32_e64 v59, 0, v61, s[42:43]
	v_add_f32_e32 v60, v68, v60
	v_add_f32_e32 v61, v69, v61
	v_add_u32_e32 v70, 10, v143
	v_add_f32_e32 v58, v60, v59
	v_add_f32_e32 v57, v57, v58
	v_add_f32_e32 v59, v63, v57
	v_add_f32_e32 v56, v56, v59
	v_add_f32_e32 v56, v120, v56
	v_add_f32_e32 v59, v116, v59
	v_add_f32_e32 v57, v117, v57
	v_add_f32_e32 v58, v76, v58
	v_exp_f32_e32 v56, v56
	v_exp_f32_e32 v62, v59
	v_exp_f32_e32 v57, v57
	v_exp_f32_e32 v63, v58
	v_pk_add_f32 v[60:61], v[60:61], v[60:61] op_sel:[0,1] op_sel_hi:[1,0]
	v_add_u32_e32 v71, 9, v143
	v_add_u32_e32 v61, 8, v143
	v_cvt_pk_bf16_f32 v56, v56, v62
	v_cvt_pk_bf16_f32 v57, v57, v63
	v_sub_f32_e32 v62, v114, v112
	v_sub_f32_e32 v63, v115, v113
	v_cmp_lt_i32_e32 vcc, v61, v28
	v_cmp_lt_i32_e64 s[46:47], v71, v28
	v_cmp_lt_i32_e64 s[48:49], v70, v29
	v_mov_b32_e32 v70, v52
	v_mov_b32_e32 v71, v54
	v_cvt_pk_bf16_f32 v59, v99, v78
	v_cndmask_b32_e32 v61, v200, v62, vcc
	v_add_u32_e32 v76, 11, v143
	v_sub_f32_e32 v68, v110, v108
; #define LAS __attribute__((address_space(3)))
; __device__ __forceinline__ void sb_unit(LAS unsigned char* lds, int wv, int lane, const Tens T, int q0, bf16_t* outp, int opitch, unsigned* nctr, int* pend) {
;     ...
;             float P = R; unsigned pk[2][8];
; #pragma unroll
;     ...
; #pragma unroll
;                 for (int g = 3; g >= 0; --g) {
;                     const float G = (l1[kk][4 * g] + l1[kk][4 * g + 1]) + (l1[kk][4 * g + 2] + l1[kk][4 * g + 3]);
;                     auto rr = __builtin_amdgcn_permlane32_swap(__float_as_uint(G), __float_as_uint(G), false, false);
;                     const float G0 = __uint_as_float(rr[0]), G1 = __uint_as_float(rr[1]);
;                     const float pre = P + (hf == 0 ? G1 : 0.f);
;                     const float s3 = pre, s2 = s3 + l1[kk][4 * g + 3], s1 = s2 + l1[kk][4 * g + 2], s0 = s1 + l1[kk][4 * g + 1];
;                     const float a0 = __builtin_amdgcn_exp2f(lb[kk][4 * g] + s0), a1 = __builtin_amdgcn_exp2f(lb[kk][4 * g + 1] + s1), a2 = __builtin_amdgcn_exp2f(lb[kk][4 * g + 2] + s2), a3 = __builtin_amdgcn_exp2f(lb[kk][4 * g + 3] + s3);
;                     pk[kk][2 * g] = cvt_pk_bf16(a0, a1); pk[kk][2 * g + 1] = cvt_pk_bf16(a2, a3);
;                     P += G0 + G1;
;                 }
;             R = P;
;             LAS unsigned char* vb = lds + (buf ? VB1 : VB0) + (4 * hf + ((lane & 15) >> 2)) * VS + (16 * ((lane >> 4) & 1) + 4 * (lane & 3)) * 2;
;             bf16x8 vfr[4][2];
; #pragma unroll
;             for (int cc = 0; cc < 4; ++cc)
; #pragma unroll
;                 for (int db = 0; db < 2; ++db) vfr[cc][db] = vfrag(vb + cc * 16 * VS + db * 64);
;             __builtin_amdgcn_sched_barrier(0);
; #pragma unroll
;             for (int cc = 0; cc < 4; ++cc) {
;                 const u32x4 pw = {pk[cc >> 1][4 * (cc & 1)], pk[cc >> 1][4 * (cc & 1) + 1], pk[cc >> 1][4 * (cc & 1) + 2], pk[cc >> 1][4 * (cc & 1) + 3]};
;                 const bf16x8 pb = __builtin_bit_cast(bf16x8, pw);
; #pragma unroll
;                 for (int db = 0; db < 2; ++db) ot[db] = __builtin_amdgcn_mfma_f32_32x32x16_bf16(vfr[cc][db], pb, ot[db], 0, 0, 0);
;             }
;             __builtin_amdgcn_sched_barrier(0);
;             done = __all(R < -46.f);
	v_sub_f32_e32 v69, v111, v109
	v_cndmask_b32_e64 v78, v200, v63, s[48:49]
	v_sub_f32_e32 v62, v62, v70
	v_sub_f32_e32 v63, v63, v71
	v_mov_b32_e32 v54, v53
	v_cndmask_b32_e32 v62, 0, v62, vcc
	v_cmp_lt_i32_e32 vcc, v76, v29
	v_sub_f32_e32 v52, v68, v54
	v_sub_f32_e32 v53, v69, v55
	v_cndmask_b32_e64 v63, 0, v63, s[48:49]
	v_cndmask_b32_e32 v53, 0, v53, vcc
	v_cndmask_b32_e64 v52, 0, v52, s[46:47]
	v_add_f32_e32 v54, v62, v52
	v_add_f32_e32 v55, v63, v53
	v_cndmask_b32_e64 v77, v200, v68, s[46:47]
	v_pk_add_f32 v[54:55], v[54:55], v[54:55] op_sel:[0,1] op_sel_hi:[1,0]
	v_cndmask_b32_e32 v70, v200, v69, vcc
	v_mov_b32_e32 v55, v54
	s_nop 1
	v_permlane32_swap_b32_e32 v54, v55
	v_cndmask_b32_e64 v62, 0, v55, s[42:43]
	v_add_f32_e32 v62, v60, v62
	v_add_f32_e32 v53, v53, v62
	v_add_f32_e32 v63, v63, v53
	v_add_f32_e32 v52, v52, v63
	v_add_f32_e32 v52, v61, v52
	v_exp_f32_e32 v110, v52
	v_add_f32_e32 v52, v77, v63
	v_exp_f32_e32 v111, v52
	v_add_f32_e32 v52, v78, v53
	v_add_u32_e32 v144, 2, v143
	v_exp_f32_e32 v113, v52
	v_add_f32_e32 v52, v70, v62
	v_exp_f32_e32 v116, v52
	v_add_f32_e32 v52, v54, v55
	v_sub_f32_e32 v54, v106, v104
	v_sub_f32_e32 v55, v107, v105
	v_cmp_lt_i32_e32 vcc, v143, v28
	v_cmp_lt_i32_e64 s[48:49], v144, v29
	v_mov_b32_e32 v68, v48
	v_mov_b32_e32 v69, v50
	v_cndmask_b32_e32 v70, v200, v54, vcc
	v_or_b32_e32 v53, 3, v143
	v_or_b32_e32 v61, 1, v143
	v_sub_f32_e32 v62, v102, v100
	v_sub_f32_e32 v63, v103, v101
	v_cndmask_b32_e64 v76, v200, v55, s[48:49]
	v_sub_f32_e32 v54, v54, v68
	v_sub_f32_e32 v55, v55, v69
	v_mov_b32_e32 v50, v49
	v_cmp_lt_i32_e64 s[46:47], v61, v28
	v_cndmask_b32_e32 v54, 0, v54, vcc
	v_cmp_lt_i32_e32 vcc, v53, v29
	v_sub_f32_e32 v48, v62, v50
	v_sub_f32_e32 v49, v63, v51
	v_cndmask_b32_e64 v55, 0, v55, s[48:49]
	v_cndmask_b32_e32 v49, 0, v49, vcc
	v_cndmask_b32_e64 v48, 0, v48, s[46:47]
	v_add_f32_e32 v50, v54, v48
	v_add_f32_e32 v51, v55, v49
	v_cndmask_b32_e64 v71, v200, v62, s[46:47]
	v_pk_add_f32 v[50:51], v[50:51], v[50:51] op_sel:[0,1] op_sel_hi:[1,0]
	v_cndmask_b32_e32 v68, v200, v63, vcc
	v_mov_b32_e32 v53, v50
	s_nop 1
	v_permlane32_swap_b32_e32 v50, v53
	v_mov_b32_e32 v61, v50
	v_cndmask_b32_e64 v51, 0, v53, s[42:43]
	v_add_f32_e32 v114, v60, v52
	v_add_f32_e32 v115, v61, v53
	s_cselect_b32 s16, 0x6800, s76
	v_add_f32_e32 v50, v114, v51
	v_add_f32_e32 v49, v49, v50
	v_add_f32_e32 v51, v55, v49
	v_add_f32_e32 v48, v48, v51
	v_add_f32_e32 v48, v70, v48
	v_exp_f32_e32 v117, v48
	v_add_f32_e32 v48, v71, v51
	v_exp_f32_e32 v118, v48
	v_add_f32_e32 v48, v76, v49
	v_exp_f32_e32 v119, v48
	v_add_f32_e32 v48, v68, v50
	v_add_u32_e32 v106, s16, v95
	v_cvt_pk_bf16_f32 v58, v79, v98
	v_exp_f32_e32 v120, v48
	ds_read_b64_tr_b16 v[48:49], v106
	ds_read_b64_tr_b16 v[50:51], v106 offset:1536
	ds_read_b64_tr_b16 v[54:55], v106 offset:1600
	ds_read_b64_tr_b16 v[52:53], v106 offset:64
	ds_read_b64_tr_b16 v[60:61], v106 offset:3072
	ds_read_b64_tr_b16 v[62:63], v106 offset:4608
	ds_read_b64_tr_b16 v[70:71], v106 offset:4672
	ds_read_b64_tr_b16 v[68:69], v106 offset:3136
	ds_read_b64_tr_b16 v[76:77], v106 offset:6144
	ds_read_b64_tr_b16 v[78:79], v106 offset:7680
	ds_read_b64_tr_b16 v[100:101], v106 offset:7744
	ds_read_b64_tr_b16 v[98:99], v106 offset:6208
	ds_read_b64_tr_b16 v[102:103], v106 offset:9216
	ds_read_b64_tr_b16 v[104:105], v106 offset:10752
	ds_read_b64_tr_b16 v[108:109], v106 offset:10816
	ds_read_b64_tr_b16 v[106:107], v106 offset:9280
	v_cvt_pk_bf16_f32 v74, v166, v163
	v_cvt_pk_bf16_f32 v66, v147, v148
	v_cvt_pk_bf16_f32 v67, v145, v146
	v_cvt_pk_bf16_f32 v112, v110, v111
	v_cvt_pk_bf16_f32 v113, v113, v116
	v_cvt_pk_bf16_f32 v110, v117, v118
	v_cvt_pk_bf16_f32 v111, v119, v120
	s_waitcnt lgkmcnt(14)
	s_nop 0
	v_mfma_f32_32x32x16_bf16 v[0:15], v[48:51], v[110:113], v[0:15]
	s_waitcnt lgkmcnt(12)
	v_mfma_f32_32x32x16_bf16 v[32:47], v[52:55], v[110:113], v[32:47]
	s_waitcnt lgkmcnt(10)
	v_mfma_f32_32x32x16_bf16 v[0:15], v[60:63], v[56:59], v[0:15]
	s_waitcnt lgkmcnt(8)
	v_mfma_f32_32x32x16_bf16 v[32:47], v[68:71], v[56:59], v[32:47]
	s_waitcnt lgkmcnt(6)
	v_mfma_f32_32x32x16_bf16 v[0:15], v[76:79], v[64:67], v[0:15]
	s_waitcnt lgkmcnt(4)
	v_mfma_f32_32x32x16_bf16 v[32:47], v[98:101], v[64:67], v[32:47]
	v_add_f32_e32 v98, v114, v115
	s_waitcnt lgkmcnt(2)
	v_mfma_f32_32x32x16_bf16 v[0:15], v[102:105], v[72:75], v[0:15]
	s_waitcnt lgkmcnt(0)
	v_mfma_f32_32x32x16_bf16 v[32:47], v[106:109], v[72:75], v[32:47]
	s_mov_b32 s16, 0xc2380000
	v_cmp_gt_f32_e32 vcc, s16, v98
	s_cmp_eq_u64 vcc, exec
	s_cselect_b64 s[16:17], -1, 0

; __device__ __forceinline__ unsigned cvt_pk_bf16(float lo, float hi) { f32x2 v = {lo, hi}; bf16x2_t b = __builtin_convertvector(v, bf16x2_t); return __builtin_bit_cast(unsigned, b); }
; __device__ __forceinline__ float swapsum(float a) { auto rr = __builtin_amdgcn_permlane32_swap(__float_as_uint(a), __float_as_uint(a), false, false); return __uint_as_float(rr[0]) + __uint_as_float(rr[1]); }
;     ...
;     l = swapsum(l);
;     if (SWA) { const float sk = sink_l2 + (ALIBI ? slope_l2 * (float)(pos[qidx] - pos_ref) : 0.f);
;         const float mnew = fmaxf(m, sk), f = __builtin_amdgcn_exp2f(m - mnew); l = l * f + __builtin_amdgcn_exp2f(sk - mnew);
; #pragma unroll
;         for (int i = 0; i < 16; ++i) { ot[0][i] *= f; ot[1][i] *= f; } }
;     const float inv = 1.f / l;
;     ...
;     else { bf16_t* op = (bf16_t*)outp + (size_t)qidx * opitch + 4 * hf + hsel * 64;
; #pragma unroll
;         for (int db = 0; db < 2; ++db)
; #pragma unroll
;             for (int g = 0; g < 4; ++g) *(u32x2*)(op + 32 * db + 8 * g) = (u32x2){cvt_pk_bf16(ot[db][4 * g] * inv, ot[db][4 * g + 1] * inv), cvt_pk_bf16(ot[db][4 * g + 2] * inv, ot[db][4 * g + 3] * inv)}; }
.LBB0_1025:
	s_or_b64 exec, exec, s[40:41]
	v_lshl_add_u64 v[0:1], v[112:113], 2, s[6:7]
	global_load_dword v0, v[0:1], off
	s_mulk_i32 s62, 0xa00
	v_mov_b32_e32 v2, v119
	s_add_u32 s3, s13, s62
	s_nop 0
	v_permlane32_swap_b32_e32 v119, v2
	s_addc_u32 s28, s31, 0
	s_lshl_b32 s20, s21, 1
	s_add_u32 s20, s3, s20
	s_addc_u32 s21, s28, 0
	s_movk_i32 s3, 0xa00
	v_ashrrev_i32_e32 v117, 31, v116
	s_waitcnt vmcnt(0)
	v_sub_u32_e32 v0, v0, v115
	v_cvt_f32_i32_e32 v251, v0
	v_mov_b32_e32 v115, v122
	v_mul_f32_e32 v0, v114, v250
	v_mul_f32_e32 v1, v115, v251
	s_nop 0
	v_add_f32_e32 v0, v0, v1
	v_max_f32_e32 v1, v172, v172
	v_max_f32_e32 v1, v1, v0
	v_sub_f32_e32 v3, v172, v1
	v_sub_f32_e32 v0, v0, v1
	v_exp_f32_e32 v4, v3
	v_exp_f32_e32 v0, v0
	v_add_f32_e32 v1, v119, v2
	v_fmac_f32_e32 v0, v1, v4
	v_div_scale_f32 v1, s[28:29], v0, v0, 1.0
	v_rcp_f32_e32 v2, v1
	s_nop 0
	v_fma_f32 v3, -v1, v2, 1.0
	v_fmac_f32_e32 v2, v3, v2
	v_div_scale_f32 v3, vcc, 1.0, v0, 1.0
	v_mul_f32_e32 v5, v3, v2
	v_fma_f32 v6, -v1, v5, v3
	v_fmac_f32_e32 v5, v6, v2
	v_fma_f32 v1, -v1, v5, v3
	v_div_fmas_f32 v1, v1, v2, v5
	v_mov_b64_e32 v[2:3], s[20:21]
	v_div_fixup_f32 v0, v1, v0, 1.0
	v_mad_i64_i32 v[2:3], s[20:21], v112, s3, v[2:3]
	v_mul_f32_e32 v6, v48, v4
	v_mul_f32_e32 v7, v49, v4
	v_mul_f32_e32 v8, v50, v4
	v_mul_f32_e32 v9, v51, v4
	v_lshl_add_u64 v[2:3], v[116:117], 1, v[2:3]
	v_mul_f32_e32 v6, v6, v0
	v_mul_f32_e32 v7, v7, v0
	v_mul_f32_e32 v8, v8, v0
	v_mul_f32_e32 v9, v9, v0
	v_lshl_add_u64 v[2:3], v[2:3], 0, s[4:5]
	v_cvt_pk_bf16_f32 v48, v6, v7
	v_cvt_pk_bf16_f32 v49, v8, v9
	v_mul_f32_e32 v6, v52, v4
	v_mul_f32_e32 v7, v53, v4
	v_mul_f32_e32 v8, v54, v4
	v_mul_f32_e32 v9, v55, v4
	v_mul_f32_e32 v6, v6, v0
	v_mul_f32_e32 v7, v7, v0
	v_mul_f32_e32 v8, v8, v0
	v_mul_f32_e32 v9, v9, v0
	v_cvt_pk_bf16_f32 v52, v6, v7
	v_cvt_pk_bf16_f32 v53, v8, v9
	v_mul_f32_e32 v6, v56, v4
	v_mul_f32_e32 v7, v57, v4
	v_mul_f32_e32 v8, v58, v4
	v_mul_f32_e32 v9, v59, v4
	v_mul_f32_e32 v6, v6, v0
	v_mul_f32_e32 v7, v7, v0
	v_mul_f32_e32 v8, v8, v0
	v_mul_f32_e32 v9, v9, v0
	v_cvt_pk_bf16_f32 v56, v6, v7
	v_cvt_pk_bf16_f32 v57, v8, v9
	v_mul_f32_e32 v6, v60, v4
	v_mul_f32_e32 v7, v61, v4
	v_mul_f32_e32 v8, v62, v4
	v_mul_f32_e32 v9, v63, v4
	v_mul_f32_e32 v6, v6, v0
	v_mul_f32_e32 v7, v7, v0
	v_mul_f32_e32 v8, v8, v0
	v_mul_f32_e32 v9, v9, v0
	v_cvt_pk_bf16_f32 v60, v6, v7
	v_cvt_pk_bf16_f32 v61, v8, v9
	v_mul_f32_e32 v6, v32, v4
	v_mul_f32_e32 v7, v33, v4
	v_mul_f32_e32 v8, v34, v4
	v_mul_f32_e32 v9, v35, v4
	v_mul_f32_e32 v6, v6, v0
	v_mul_f32_e32 v7, v7, v0
	v_mul_f32_e32 v8, v8, v0
	v_mul_f32_e32 v9, v9, v0
	v_cvt_pk_bf16_f32 v50, v6, v7
	v_cvt_pk_bf16_f32 v51, v8, v9
	v_mul_f32_e32 v6, v36, v4
	v_mul_f32_e32 v7, v37, v4
	v_mul_f32_e32 v8, v38, v4
	v_mul_f32_e32 v9, v39, v4
	v_mul_f32_e32 v6, v6, v0
	v_mul_f32_e32 v7, v7, v0
	v_mul_f32_e32 v8, v8, v0
	v_mul_f32_e32 v9, v9, v0
	v_cvt_pk_bf16_f32 v54, v6, v7
	v_cvt_pk_bf16_f32 v55, v8, v9
	v_mul_f32_e32 v6, v40, v4
	v_mul_f32_e32 v7, v41, v4
	v_mul_f32_e32 v8, v42, v4
	v_mul_f32_e32 v9, v43, v4
	v_mul_f32_e32 v6, v6, v0
	v_mul_f32_e32 v7, v7, v0
	v_mul_f32_e32 v8, v8, v0
	v_mul_f32_e32 v9, v9, v0
	v_cvt_pk_bf16_f32 v58, v6, v7
	v_cvt_pk_bf16_f32 v59, v8, v9
	v_mul_f32_e32 v6, v44, v4
	v_mul_f32_e32 v7, v45, v4
	v_mul_f32_e32 v5, v47, v4
	v_mul_f32_e32 v4, v46, v4
	v_mul_f32_e32 v6, v6, v0
	v_mul_f32_e32 v7, v7, v0
	v_mul_f32_e32 v1, v5, v0
	v_mul_f32_e32 v0, v4, v0
	v_cvt_pk_bf16_f32 v62, v6, v7
	v_cvt_pk_bf16_f32 v63, v0, v1
	s_nop 1
	v_permlane32_swap_b32_e32 v48, v50
	v_permlane32_swap_b32_e32 v49, v51
	v_permlane32_swap_b32_e32 v52, v54
	v_permlane32_swap_b32_e32 v53, v55
	v_permlane32_swap_b32_e32 v56, v58
	v_permlane32_swap_b32_e32 v57, v59
	v_permlane32_swap_b32_e32 v60, v62
	v_permlane32_swap_b32_e32 v61, v63
	v_mbcnt_lo_u32_b32 v8, -1, 0
	v_mbcnt_hi_u32_b32 v8, -1, v8
	v_lshrrev_b32_e32 v8, 5, v8
	v_mul_u32_u24_e32 v8, 56, v8
	v_add_co_u32_e32 v2, vcc, v2, v8
	s_nop 1
	v_addc_co_u32_e32 v3, vcc, 0, v3, vcc
	global_store_dwordx4 v[2:3], v[48:51], off offset:1024
	global_store_dwordx4 v[2:3], v[52:55], off offset:1040
	global_store_dwordx4 v[2:3], v[56:59], off offset:1056
	global_store_dwordx4 v[2:3], v[60:63], off offset:1072

.LBB0_1044:
	v_max_f32_e32 v64, v17, v17
	v_max_f32_e32 v65, v1, v1
	v_max_f32_e32 v64, v65, v64
	v_max_f32_e32 v65, v18, v18
	v_max_f32_e32 v66, v2, v2
	v_max_f32_e32 v65, v66, v65
	v_max_f32_e32 v66, v19, v19
	v_max_f32_e32 v67, v3, v3
	v_max_f32_e32 v66, v67, v66
	v_max3_f32 v64, v0, v16, v64
	v_max3_f32 v64, v64, v65, v66
	v_max_f32_e32 v65, v20, v20
	v_max_f32_e32 v66, v4, v4
	v_max_f32_e32 v65, v66, v65
	v_max_f32_e32 v66, v21, v21
	v_max_f32_e32 v67, v5, v5
	v_max_f32_e32 v66, v67, v66
	v_max3_f32 v64, v64, v65, v66
	v_max_f32_e32 v65, v22, v22
	v_max_f32_e32 v66, v6, v6
	v_max_f32_e32 v65, v66, v65
	v_max_f32_e32 v66, v23, v23
	v_max_f32_e32 v67, v7, v7
	v_max_f32_e32 v66, v67, v66
	v_max3_f32 v64, v64, v65, v66
	v_max_f32_e32 v65, v24, v24
	v_max_f32_e32 v66, v8, v8
	v_max_f32_e32 v65, v66, v65
	v_max_f32_e32 v66, v25, v25
	v_max_f32_e32 v67, v9, v9
	v_max_f32_e32 v66, v67, v66
	v_max3_f32 v64, v64, v65, v66
	v_max_f32_e32 v65, v26, v26
	v_max_f32_e32 v66, v10, v10
	v_max_f32_e32 v65, v66, v65
	v_max_f32_e32 v66, v27, v27
	v_max_f32_e32 v67, v11, v11
	v_max_f32_e32 v66, v67, v66
	v_max3_f32 v64, v64, v65, v66
	v_max_f32_e32 v65, v28, v28
	v_max_f32_e32 v66, v12, v12
	v_max_f32_e32 v65, v66, v65
	v_max_f32_e32 v66, v29, v29
	v_max_f32_e32 v67, v13, v13
	v_max_f32_e32 v66, v67, v66
	v_max3_f32 v64, v64, v65, v66
	v_max_f32_e32 v65, v30, v30
	v_max_f32_e32 v66, v14, v14
	v_max_f32_e32 v65, v66, v65
	v_max_f32_e32 v66, v79, v79
	v_max_f32_e32 v67, v15, v15
	v_max_f32_e32 v66, v67, v66
	v_max3_f32 v64, v64, v65, v66
	v_mov_b32_e32 v65, v64
	s_nop 1
	v_permlane32_swap_b32_e32 v64, v65
	v_max_f32_e32 v65, v65, v65
	v_max_f32_e32 v64, v64, v64
	v_max_f32_e32 v64, v64, v65
	v_add_f32_e32 v65, 0x41000000, v172
	v_cmp_gt_f32_e32 vcc, v64, v65
	s_cbranch_vccz .LBB0_1046
	v_max_f32_e32 v64, v64, v64
	v_max_f32_e32 v65, v172, v172
	v_max_f32_e32 v65, v65, v64
	v_sub_f32_e32 v64, v172, v65
	v_exp_f32_e32 v64, v64
	v_mov_b32_e32 v172, v65
	v_mul_f32_e32 v62, v62, v64
	v_mul_f32_e32 v63, v63, v64
	v_mul_f32_e32 v60, v60, v64
	v_mul_f32_e32 v61, v61, v64
	v_mul_f32_e32 v58, v58, v64
	v_mul_f32_e32 v59, v59, v64
	v_mul_f32_e32 v56, v56, v64
	v_mul_f32_e32 v57, v57, v64
	v_mul_f32_e32 v54, v54, v64
	v_mul_f32_e32 v55, v55, v64
	v_mul_f32_e32 v52, v52, v64
	v_mul_f32_e32 v53, v53, v64
	v_mul_f32_e32 v50, v50, v64
	v_mul_f32_e32 v51, v51, v64
	v_mul_f32_e32 v48, v48, v64
	v_mul_f32_e32 v49, v49, v64
	v_mul_f32_e32 v46, v46, v64
	v_mul_f32_e32 v47, v47, v64
	v_mul_f32_e32 v44, v44, v64
	v_mul_f32_e32 v45, v45, v64
	v_mul_f32_e32 v42, v42, v64
	v_mul_f32_e32 v43, v43, v64
	v_mul_f32_e32 v40, v40, v64
	v_mul_f32_e32 v41, v41, v64
	v_mul_f32_e32 v38, v38, v64
	v_mul_f32_e32 v39, v39, v64
	v_mul_f32_e32 v36, v36, v64
	v_mul_f32_e32 v37, v37, v64
	v_mul_f32_e32 v34, v34, v64
	v_mul_f32_e32 v35, v35, v64
	v_mul_f32_e32 v32, v32, v64
	v_mul_f32_e32 v33, v33, v64
	v_mul_f32_e32 v119, v119, v64
